# K-loop edge edits on top of best: s_setprio 1 issued before the pre-MFMA barrier; post-MFMA scalar/address updates moved into the MFMA shadow (pure moves, placement preserved)
# speedup vs baseline: 1.0075x; 1.0033x over previous
; #define G8_STAGE(bufoff, gbase, voff) do { _Pragma("unroll") for (int _i = 0; _i < 2; ++_i) \
;         __builtin_amdgcn_global_load_lds((const unsigned*)((const char*)(gbase) + (voff)[_i]), (LAS unsigned*)(lds + (bufoff) + ldsw + _i * 8192), 16, 0, 0); } while (0)
; #define G8_LDA(dst, b, h) do { _Pragma("unroll") for (int m = 0; m < 4; ++m) _Pragma("unroll") for (int k = 0; k < 2; ++k) dst[m][k] = *(const LAS bf16x8*)(lds + G8_SA(b, h) + aoff + m * 2048 + k * 1024); } while (0)
; #define G8_LDB(dst, b, h) do { _Pragma("unroll") for (int n = 0; n < 2; ++n) _Pragma("unroll") for (int k = 0; k < 2; ++k) dst[n][k] = *(const LAS bf16x8*)(lds + G8_SB(b, h) + boff + n * 2048 + k * 1024); } while (0)
; #define G8_MMA(ai, bj, At, Bt) do { __builtin_amdgcn_s_setprio(1); _Pragma("unroll") for (int m = 0; m < 4; ++m) _Pragma("unroll") for (int n = 0; n < 2; ++n) _Pragma("unroll") for (int k = 0; k < 2; ++k) \
;         acc[ai][bj][m][n] = __builtin_amdgcn_mfma_f32_16x16x32_bf16(Bt[n][k], At[m][k], acc[ai][bj][m][n], 0, 0, 0); __builtin_amdgcn_s_setprio(0); } while (0)
; #define G8_WAIT_L(n) asm volatile("s_waitcnt lgkmcnt(" #n ")" ::: "memory")
; #define G8_BAR __builtin_amdgcn_s_barrier()
; template <class Epi, class Sched>
; __device__ __forceinline__ void gemm_phase(LAS unsigned char* lds, const int K, const Sched& S, const Epi& E) {
;     ...
;         const bool has_next = S.next(ui + 1, nxt);
;         const char* nA = has_next ? nxt.A : cA; const char* nB = has_next ? nxt.B : cB;
; #pragma unroll 1
;         for (int t = 0; t < nt; t += 2) {
;             const bool last = (t == nt - 2);
;             const char* a1 = cA + (size_t)(t + 1) * kstep;
;             const char* a2 = last ? nA : cA + (size_t)(t + 2) * kstep; const char* b2 = last ? nB : cB + (size_t)(t + 2) * kstep;
;             const char* a3 = a2 + kstep; const char* b3 = b2 + kstep;
;             G8_LDB(B0, 0, 0); G8_SCHED; G8_LDA(At, 0, 0); G8_STAGE(G8_SA(1, 1), a1, oc[1]);
;             if (last && has_next) S.aoff(nxt, tid, oc);
;             G8_WAIT_L(8); G8_BAR; G8_WAIT_L(0); G8_MMA(0, 0, At, B0); G8_BAR; G8_SCHED;
;             G8_LDB(B1, 0, 1); G8_STAGE(G8_SB(0, 0), b2, voffB);
;             G8_BAR; G8_WAIT_L(0); G8_MMA(0, 1, At, B1); G8_BAR;
;             G8_LDA(At, 0, 1); G8_STAGE(G8_SA(0, 0), a2, oc[0]);
;             G8_BAR; G8_WAIT_L(0); G8_MMA(1, 0, At, B0); G8_BAR; G8_SCHED;
.LBB0_320:
	s_add_u32 s36, s2, 0x100
	s_addc_u32 s37, s3, 0
	s_add_i32 s82, 0, 0x10000
	v_add_u32_e32 v0, s82, v145
	ds_read_b128 v[154:157], v0
	ds_read_b128 v[158:161], v0 offset:1024
	ds_read_b128 v[162:165], v0 offset:2048
	ds_read_b128 v[166:169], v0 offset:3072
	s_cmp_eq_u32 s11, 12
	s_cselect_b32 s49, s43, s37
	s_cselect_b32 s48, s42, s36
	s_cselect_b32 s47, s45, s9
	s_cselect_b32 s46, s44, s5
	v_lshl_add_u64 v[150:151], s[2:3], 0, v[148:149]
	s_add_i32 m0, s58, 0xc000
	ds_read_b128 v[170:173], v153
	ds_read_b128 v[174:177], v153 offset:1024
	ds_read_b128 v[178:181], v153 offset:2048
	ds_read_b128 v[182:185], v153 offset:3072
	ds_read_b128 v[186:189], v153 offset:4096
	ds_read_b128 v[190:193], v153 offset:5120
	ds_read_b128 v[194:197], v153 offset:6144
	ds_read_b128 v[198:201], v153 offset:7168
	global_load_lds_dwordx4 v[150:151], off
	v_lshl_add_u64 v[150:151], s[2:3], 0, v[146:147]
	s_add_i32 m0, s58, 0xe000
	s_nop 0
	global_load_lds_dwordx4 v[150:151], off
	s_waitcnt lgkmcnt(8)
	s_setprio 1
	s_barrier
	s_waitcnt lgkmcnt(0)
	s_waitcnt lgkmcnt(0)
	v_mfma_f32_16x16x32_bf16 v[126:129], v[154:157], v[170:173], v[126:129]
	v_mfma_f32_16x16x32_bf16 v[122:125], v[162:165], v[170:173], v[122:125]
	v_mfma_f32_16x16x32_bf16 v[110:113], v[154:157], v[178:181], v[110:113]
	v_mfma_f32_16x16x32_bf16 v[106:109], v[162:165], v[178:181], v[106:109]
	v_mfma_f32_16x16x32_bf16 v[94:97], v[154:157], v[186:189], v[94:97]
	v_mfma_f32_16x16x32_bf16 v[90:93], v[162:165], v[186:189], v[90:93]
	v_mfma_f32_16x16x32_bf16 v[78:81], v[154:157], v[194:197], v[78:81]
	v_mfma_f32_16x16x32_bf16 v[74:77], v[162:165], v[194:197], v[74:77]
	v_mfma_f32_16x16x32_bf16 v[126:129], v[158:161], v[174:177], v[126:129]
	v_mfma_f32_16x16x32_bf16 v[122:125], v[166:169], v[174:177], v[122:125]
	v_mfma_f32_16x16x32_bf16 v[110:113], v[158:161], v[182:185], v[110:113]
	v_mfma_f32_16x16x32_bf16 v[106:109], v[166:169], v[182:185], v[106:109]
	v_mfma_f32_16x16x32_bf16 v[94:97], v[158:161], v[190:193], v[94:97]
	v_mfma_f32_16x16x32_bf16 v[90:93], v[166:169], v[190:193], v[90:93]
	v_mfma_f32_16x16x32_bf16 v[78:81], v[158:161], v[198:201], v[78:81]
	v_mfma_f32_16x16x32_bf16 v[74:77], v[166:169], v[198:201], v[74:77]
	s_setprio 0
	s_barrier
	s_add_i32 s83, 0, 0x14000
	s_add_i32 s2, s82, s57
	v_add_u32_e32 v0, s83, v145
	v_lshl_add_u64 v[150:151], s[46:47], 0, v[132:133]
	s_mov_b32 m0, s2
	ds_read_b128 v[216:219], v0
	ds_read_b128 v[220:223], v0 offset:1024
	ds_read_b128 v[224:227], v0 offset:2048
	ds_read_b128 v[228:231], v0 offset:3072
	global_load_lds_dwordx4 v[150:151], off
	v_lshl_add_u64 v[232:233], s[46:47], 0, v[134:135]
	s_add_i32 m0, s2, 0x2000
	s_nop 0
	global_load_lds_dwordx4 v[232:233], off
	s_setprio 1
	s_barrier
	s_waitcnt lgkmcnt(0)
	s_waitcnt lgkmcnt(0)
	v_mfma_f32_16x16x32_bf16 v[118:121], v[216:219], v[170:173], v[118:121]
	v_mfma_f32_16x16x32_bf16 v[114:117], v[224:227], v[170:173], v[114:117]
	v_mfma_f32_16x16x32_bf16 v[102:105], v[216:219], v[178:181], v[102:105]
	v_mfma_f32_16x16x32_bf16 v[98:101], v[224:227], v[178:181], v[98:101]
	v_mfma_f32_16x16x32_bf16 v[86:89], v[216:219], v[186:189], v[86:89]
	v_mfma_f32_16x16x32_bf16 v[82:85], v[224:227], v[186:189], v[82:85]
	v_mfma_f32_16x16x32_bf16 v[70:73], v[216:219], v[194:197], v[70:73]
	v_mfma_f32_16x16x32_bf16 v[66:69], v[224:227], v[194:197], v[66:69]
	v_mfma_f32_16x16x32_bf16 v[118:121], v[220:223], v[174:177], v[118:121]
	s_mov_b32 m0, s58
	v_mfma_f32_16x16x32_bf16 v[114:117], v[228:231], v[174:177], v[114:117]
	v_lshl_add_u64 v[234:235], s[48:49], 0, v[136:137]
	v_mfma_f32_16x16x32_bf16 v[102:105], v[220:223], v[182:185], v[102:105]
	v_mfma_f32_16x16x32_bf16 v[98:101], v[228:231], v[182:185], v[98:101]
	v_mfma_f32_16x16x32_bf16 v[86:89], v[220:223], v[190:193], v[86:89]
	v_mfma_f32_16x16x32_bf16 v[82:85], v[228:231], v[190:193], v[82:85]
	v_mfma_f32_16x16x32_bf16 v[70:73], v[220:223], v[198:201], v[70:73]
	v_mfma_f32_16x16x32_bf16 v[66:69], v[228:231], v[198:201], v[66:69]
	s_setprio 0
	s_barrier
	ds_read_b128 v[170:173], v153 offset:16384
	ds_read_b128 v[174:177], v153 offset:17408
	ds_read_b128 v[178:181], v153 offset:18432
	ds_read_b128 v[182:185], v153 offset:19456
	ds_read_b128 v[186:189], v153 offset:20480
	ds_read_b128 v[190:193], v153 offset:21504
	ds_read_b128 v[194:197], v153 offset:22528
	ds_read_b128 v[198:201], v153 offset:23552
	global_load_lds_dwordx4 v[234:235], off
	v_lshl_add_u64 v[236:237], s[48:49], 0, v[140:141]
	s_mov_b32 m0, s59
	s_nop 0
	global_load_lds_dwordx4 v[236:237], off
	s_setprio 1
	s_barrier
	s_waitcnt lgkmcnt(0)
	s_waitcnt lgkmcnt(0)
	v_mfma_f32_16x16x32_bf16 v[62:65], v[154:157], v[170:173], v[62:65]
	v_mfma_f32_16x16x32_bf16 v[58:61], v[162:165], v[170:173], v[58:61]
	v_mfma_f32_16x16x32_bf16 v[46:49], v[154:157], v[178:181], v[46:49]
	v_mfma_f32_16x16x32_bf16 v[42:45], v[162:165], v[178:181], v[42:45]
	v_mfma_f32_16x16x32_bf16 v[30:33], v[154:157], v[186:189], v[30:33]
	v_mfma_f32_16x16x32_bf16 v[26:29], v[162:165], v[186:189], v[26:29]
	v_mfma_f32_16x16x32_bf16 v[14:17], v[154:157], v[194:197], v[14:17]
	v_mfma_f32_16x16x32_bf16 v[10:13], v[162:165], v[194:197], v[10:13]
	v_mfma_f32_16x16x32_bf16 v[62:65], v[158:161], v[174:177], v[62:65]
	v_mfma_f32_16x16x32_bf16 v[58:61], v[166:169], v[174:177], v[58:61]
	v_mfma_f32_16x16x32_bf16 v[46:49], v[158:161], v[182:185], v[46:49]
	v_mfma_f32_16x16x32_bf16 v[42:45], v[166:169], v[182:185], v[42:45]
	v_mfma_f32_16x16x32_bf16 v[30:33], v[158:161], v[190:193], v[30:33]
	v_mfma_f32_16x16x32_bf16 v[26:29], v[166:169], v[190:193], v[26:29]
	v_mfma_f32_16x16x32_bf16 v[14:17], v[158:161], v[198:201], v[14:17]
	v_mfma_f32_16x16x32_bf16 v[10:13], v[166:169], v[198:201], v[10:13]
	s_setprio 0
	s_barrier
; #define G8_STAGE(bufoff, gbase, voff) do { _Pragma("unroll") for (int _i = 0; _i < 2; ++_i) \
;         __builtin_amdgcn_global_load_lds((const unsigned*)((const char*)(gbase) + (voff)[_i]), (LAS unsigned*)(lds + (bufoff) + ldsw + _i * 8192), 16, 0, 0); } while (0)
; #define G8_LDA(dst, b, h) do { _Pragma("unroll") for (int m = 0; m < 4; ++m) _Pragma("unroll") for (int k = 0; k < 2; ++k) dst[m][k] = *(const LAS bf16x8*)(lds + G8_SA(b, h) + aoff + m * 2048 + k * 1024); } while (0)
; #define G8_LDB(dst, b, h) do { _Pragma("unroll") for (int n = 0; n < 2; ++n) _Pragma("unroll") for (int k = 0; k < 2; ++k) dst[n][k] = *(const LAS bf16x8*)(lds + G8_SB(b, h) + boff + n * 2048 + k * 1024); } while (0)
; #define G8_MMA(ai, bj, At, Bt) do { __builtin_amdgcn_s_setprio(1); _Pragma("unroll") for (int m = 0; m < 4; ++m) _Pragma("unroll") for (int n = 0; n < 2; ++n) _Pragma("unroll") for (int k = 0; k < 2; ++k) \
;         acc[ai][bj][m][n] = __builtin_amdgcn_mfma_f32_16x16x32_bf16(Bt[n][k], At[m][k], acc[ai][bj][m][n], 0, 0, 0); __builtin_amdgcn_s_setprio(0); } while (0)
; #define G8_WAIT_V(n) asm volatile("s_waitcnt vmcnt(" #n ")" ::: "memory")
; #define G8_WAIT_L(n) asm volatile("s_waitcnt lgkmcnt(" #n ")" ::: "memory")
; #define G8_BAR __builtin_amdgcn_s_barrier()
; #define G8_SCHED __builtin_amdgcn_sched_barrier(0)
; template <class Epi, class Sched>
; __device__ __forceinline__ void gemm_phase(LAS unsigned char* lds, const int K, const Sched& S, const Epi& E) {
;     ...
;             G8_STAGE(G8_SB(0, 1), b2 + hstep, voffB);
;             G8_WAIT_V(6); G8_BAR; G8_MMA(1, 1, At, B1); G8_BAR;
;             G8_LDB(B0, 1, 0); G8_SCHED; G8_LDA(At, 1, 0); G8_STAGE(G8_SA(0, 1), a2, oc[1]);
;             G8_WAIT_L(8); G8_BAR; G8_WAIT_L(0); G8_MMA(0, 0, At, B0); G8_BAR; G8_SCHED;
;             G8_LDB(B1, 1, 1); G8_STAGE(G8_SB(1, 0), b3, voffB);
;             G8_BAR; G8_WAIT_L(0); G8_MMA(0, 1, At, B1); G8_BAR;
	s_add_u32 s2, s46, 0x40000
	s_addc_u32 s3, s47, 0
	s_add_i32 s82, s83, s57
	v_lshl_add_u64 v[154:155], s[2:3], 0, v[132:133]
	s_mov_b32 m0, s82
	s_nop 0
	global_load_lds_dwordx4 v[154:155], off
	v_lshl_add_u64 v[154:155], s[2:3], 0, v[134:135]
	s_add_i32 m0, s82, 0x2000
	s_nop 0
	global_load_lds_dwordx4 v[154:155], off
	s_waitcnt vmcnt(6)
	s_setprio 1
	s_barrier
	v_mfma_f32_16x16x32_bf16 v[54:57], v[216:219], v[170:173], v[54:57]
	v_mfma_f32_16x16x32_bf16 v[50:53], v[224:227], v[170:173], v[50:53]
	v_mfma_f32_16x16x32_bf16 v[38:41], v[216:219], v[178:181], v[38:41]
	v_mfma_f32_16x16x32_bf16 v[34:37], v[224:227], v[178:181], v[34:37]
	v_mfma_f32_16x16x32_bf16 v[22:25], v[216:219], v[186:189], v[22:25]
	v_mfma_f32_16x16x32_bf16 v[18:21], v[224:227], v[186:189], v[18:21]
	v_mfma_f32_16x16x32_bf16 v[6:9], v[216:219], v[194:197], v[6:9]
	v_mfma_f32_16x16x32_bf16 v[2:5], v[224:227], v[194:197], v[2:5]
	v_mfma_f32_16x16x32_bf16 v[54:57], v[220:223], v[174:177], v[54:57]
	s_add_i32 s2, 0, 0x18000
	v_mfma_f32_16x16x32_bf16 v[50:53], v[228:231], v[174:177], v[50:53]
	v_add_u32_e32 v0, s2, v145
	v_mfma_f32_16x16x32_bf16 v[38:41], v[220:223], v[182:185], v[38:41]
	v_mfma_f32_16x16x32_bf16 v[34:37], v[228:231], v[182:185], v[34:37]
	v_mfma_f32_16x16x32_bf16 v[22:25], v[220:223], v[190:193], v[22:25]
	v_mfma_f32_16x16x32_bf16 v[18:21], v[228:231], v[190:193], v[18:21]
	v_mfma_f32_16x16x32_bf16 v[6:9], v[220:223], v[198:201], v[6:9]
	v_mfma_f32_16x16x32_bf16 v[2:5], v[228:231], v[198:201], v[2:5]
	s_setprio 0
	s_barrier
	ds_read_b128 v[154:157], v0
	ds_read_b128 v[158:161], v0 offset:1024
	ds_read_b128 v[162:165], v0 offset:2048
	ds_read_b128 v[166:169], v0 offset:3072
	s_mov_b32 m0, s60
	v_lshl_add_u64 v[216:217], s[48:49], 0, v[138:139]
	ds_read_b128 v[170:173], v153 offset:32768
	ds_read_b128 v[174:177], v153 offset:33792
	ds_read_b128 v[178:181], v153 offset:34816
	ds_read_b128 v[182:185], v153 offset:35840
	ds_read_b128 v[186:189], v153 offset:36864
	ds_read_b128 v[190:193], v153 offset:37888
	ds_read_b128 v[194:197], v153 offset:38912
	ds_read_b128 v[198:201], v153 offset:39936
	global_load_lds_dwordx4 v[216:217], off
	v_lshl_add_u64 v[216:217], s[48:49], 0, v[142:143]
	s_mov_b32 m0, s61
	s_nop 0
	global_load_lds_dwordx4 v[216:217], off
	s_waitcnt lgkmcnt(8)
	s_setprio 1
	s_barrier
	s_waitcnt lgkmcnt(0)
	s_waitcnt lgkmcnt(0)
	v_mfma_f32_16x16x32_bf16 v[126:129], v[154:157], v[170:173], v[126:129]
	v_mfma_f32_16x16x32_bf16 v[122:125], v[162:165], v[170:173], v[122:125]
	v_mfma_f32_16x16x32_bf16 v[110:113], v[154:157], v[178:181], v[110:113]
	v_mfma_f32_16x16x32_bf16 v[106:109], v[162:165], v[178:181], v[106:109]
	v_mfma_f32_16x16x32_bf16 v[94:97], v[154:157], v[186:189], v[94:97]
	v_mfma_f32_16x16x32_bf16 v[90:93], v[162:165], v[186:189], v[90:93]
	v_mfma_f32_16x16x32_bf16 v[78:81], v[154:157], v[194:197], v[78:81]
	v_mfma_f32_16x16x32_bf16 v[74:77], v[162:165], v[194:197], v[74:77]
	v_mfma_f32_16x16x32_bf16 v[126:129], v[158:161], v[174:177], v[126:129]
	v_mfma_f32_16x16x32_bf16 v[122:125], v[166:169], v[174:177], v[122:125]
	v_mfma_f32_16x16x32_bf16 v[110:113], v[158:161], v[182:185], v[110:113]
	v_mfma_f32_16x16x32_bf16 v[106:109], v[166:169], v[182:185], v[106:109]
	v_mfma_f32_16x16x32_bf16 v[94:97], v[158:161], v[190:193], v[94:97]
	v_mfma_f32_16x16x32_bf16 v[90:93], v[166:169], v[190:193], v[90:93]
	v_mfma_f32_16x16x32_bf16 v[78:81], v[158:161], v[198:201], v[78:81]
	v_mfma_f32_16x16x32_bf16 v[74:77], v[166:169], v[198:201], v[74:77]
	s_setprio 0
	s_barrier
	s_add_i32 s48, 0, 0x1c000
	s_add_i32 s2, s2, s57
	v_add_u32_e32 v0, s48, v145
	v_lshl_add_u64 v[150:151], v[150:151], 0, s[18:19]
	s_mov_b32 m0, s2
	ds_read_b128 v[216:219], v0
	ds_read_b128 v[220:223], v0 offset:1024
	ds_read_b128 v[224:227], v0 offset:2048
	ds_read_b128 v[228:231], v0 offset:3072
	global_load_lds_dwordx4 v[150:151], off
	v_lshl_add_u64 v[150:151], v[232:233], 0, s[18:19]
	s_add_i32 m0, s2, 0x2000
	s_nop 0
	global_load_lds_dwordx4 v[150:151], off
	s_setprio 1
	s_barrier
	s_waitcnt lgkmcnt(0)
	s_waitcnt lgkmcnt(0)
	v_mfma_f32_16x16x32_bf16 v[118:121], v[216:219], v[170:173], v[118:121]
	v_mfma_f32_16x16x32_bf16 v[114:117], v[224:227], v[170:173], v[114:117]
	v_mfma_f32_16x16x32_bf16 v[102:105], v[216:219], v[178:181], v[102:105]
	v_mfma_f32_16x16x32_bf16 v[98:101], v[224:227], v[178:181], v[98:101]
	v_mfma_f32_16x16x32_bf16 v[86:89], v[216:219], v[186:189], v[86:89]
	v_mfma_f32_16x16x32_bf16 v[82:85], v[224:227], v[186:189], v[82:85]
	v_mfma_f32_16x16x32_bf16 v[70:73], v[216:219], v[194:197], v[70:73]
	v_mfma_f32_16x16x32_bf16 v[66:69], v[224:227], v[194:197], v[66:69]
	v_mfma_f32_16x16x32_bf16 v[118:121], v[220:223], v[174:177], v[118:121]
	s_mov_b32 m0, s64
	v_mfma_f32_16x16x32_bf16 v[114:117], v[228:231], v[174:177], v[114:117]
	v_lshl_add_u64 v[150:151], v[234:235], 0, s[18:19]
	v_mfma_f32_16x16x32_bf16 v[102:105], v[220:223], v[182:185], v[102:105]
	v_mfma_f32_16x16x32_bf16 v[98:101], v[228:231], v[182:185], v[98:101]
	v_mfma_f32_16x16x32_bf16 v[86:89], v[220:223], v[190:193], v[86:89]
	v_mfma_f32_16x16x32_bf16 v[82:85], v[228:231], v[190:193], v[82:85]
	v_mfma_f32_16x16x32_bf16 v[70:73], v[220:223], v[198:201], v[70:73]
	v_mfma_f32_16x16x32_bf16 v[66:69], v[228:231], v[198:201], v[66:69]
	s_setprio 0
	s_barrier
; #define G8_STAGE(bufoff, gbase, voff) do { _Pragma("unroll") for (int _i = 0; _i < 2; ++_i) \
;         __builtin_amdgcn_global_load_lds((const unsigned*)((const char*)(gbase) + (voff)[_i]), (LAS unsigned*)(lds + (bufoff) + ldsw + _i * 8192), 16, 0, 0); } while (0)
; #define G8_LDA(dst, b, h) do { _Pragma("unroll") for (int m = 0; m < 4; ++m) _Pragma("unroll") for (int k = 0; k < 2; ++k) dst[m][k] = *(const LAS bf16x8*)(lds + G8_SA(b, h) + aoff + m * 2048 + k * 1024); } while (0)
; #define G8_MMA(ai, bj, At, Bt) do { __builtin_amdgcn_s_setprio(1); _Pragma("unroll") for (int m = 0; m < 4; ++m) _Pragma("unroll") for (int n = 0; n < 2; ++n) _Pragma("unroll") for (int k = 0; k < 2; ++k) \
;         acc[ai][bj][m][n] = __builtin_amdgcn_mfma_f32_16x16x32_bf16(Bt[n][k], At[m][k], acc[ai][bj][m][n], 0, 0, 0); __builtin_amdgcn_s_setprio(0); } while (0)
; #define G8_WAIT_V(n) asm volatile("s_waitcnt vmcnt(" #n ")" ::: "memory")
; #define G8_WAIT_L(n) asm volatile("s_waitcnt lgkmcnt(" #n ")" ::: "memory")
; #define G8_BAR __builtin_amdgcn_s_barrier()
; #define G8_SCHED __builtin_amdgcn_sched_barrier(0)
; __device__ __forceinline__ f32x4 gelu4(const f32x4 x) {
;     const f32x4 t = x * ((x * x) * (-0.10294323886f) + (-2.30220819813f)); f32x4 d;
; #pragma unroll
;     for (int e = 0; e < 4; ++e) d[e] = __builtin_amdgcn_exp2f(t[e]);
;     d = d + 1.f;
; #pragma unroll
;     for (int e = 0; e < 4; ++e) d[e] = __builtin_amdgcn_rcpf(d[e]);
;     return x * d; }
; template <class Epi, class Sched>
; __device__ __forceinline__ void gemm_phase(LAS unsigned char* lds, const int K, const Sched& S, const Epi& E) {
;     ...
;             G8_LDA(At, 1, 1); G8_STAGE(G8_SA(1, 0), a3, oc[0]);
;             G8_BAR; G8_WAIT_L(0); G8_MMA(1, 0, At, B0); G8_BAR; G8_SCHED;
;             G8_STAGE(G8_SB(1, 1), b3 + hstep, voffB);
;             G8_WAIT_V(6); G8_BAR; G8_MMA(1, 1, At, B1); G8_BAR;
;         }
	ds_read_b128 v[170:173], v153 offset:49152
	ds_read_b128 v[174:177], v153 offset:50176
	ds_read_b128 v[178:181], v153 offset:51200
	ds_read_b128 v[182:185], v153 offset:52224
	ds_read_b128 v[186:189], v153 offset:53248
	ds_read_b128 v[190:193], v153 offset:54272
	ds_read_b128 v[194:197], v153 offset:55296
	ds_read_b128 v[198:201], v153 offset:56320
	global_load_lds_dwordx4 v[150:151], off
	v_lshl_add_u64 v[150:151], v[236:237], 0, s[18:19]
	s_mov_b32 m0, s65
	s_nop 0
	global_load_lds_dwordx4 v[150:151], off
	s_setprio 1
	s_barrier
	s_waitcnt lgkmcnt(0)
	s_waitcnt lgkmcnt(0)
	v_mfma_f32_16x16x32_bf16 v[62:65], v[154:157], v[170:173], v[62:65]
	v_mfma_f32_16x16x32_bf16 v[58:61], v[162:165], v[170:173], v[58:61]
	v_mfma_f32_16x16x32_bf16 v[46:49], v[154:157], v[178:181], v[46:49]
	v_mfma_f32_16x16x32_bf16 v[42:45], v[162:165], v[178:181], v[42:45]
	v_mfma_f32_16x16x32_bf16 v[30:33], v[154:157], v[186:189], v[30:33]
	v_mfma_f32_16x16x32_bf16 v[26:29], v[162:165], v[186:189], v[26:29]
	v_mfma_f32_16x16x32_bf16 v[14:17], v[154:157], v[194:197], v[14:17]
	v_mfma_f32_16x16x32_bf16 v[10:13], v[162:165], v[194:197], v[10:13]
	v_mfma_f32_16x16x32_bf16 v[62:65], v[158:161], v[174:177], v[62:65]
	v_mfma_f32_16x16x32_bf16 v[58:61], v[166:169], v[174:177], v[58:61]
	v_mfma_f32_16x16x32_bf16 v[46:49], v[158:161], v[182:185], v[46:49]
	v_mfma_f32_16x16x32_bf16 v[42:45], v[166:169], v[182:185], v[42:45]
	v_mfma_f32_16x16x32_bf16 v[30:33], v[158:161], v[190:193], v[30:33]
	v_mfma_f32_16x16x32_bf16 v[26:29], v[166:169], v[190:193], v[26:29]
	v_mfma_f32_16x16x32_bf16 v[14:17], v[158:161], v[198:201], v[14:17]
	v_mfma_f32_16x16x32_bf16 v[10:13], v[166:169], v[198:201], v[10:13]
	s_setprio 0
	s_barrier
	s_add_u32 s2, s46, 0x40080
	s_addc_u32 s3, s47, 0
	s_add_i32 s46, s48, s57
	v_lshl_add_u64 v[150:151], s[2:3], 0, v[132:133]
	s_mov_b32 m0, s46
	s_nop 0
	global_load_lds_dwordx4 v[150:151], off
	v_lshl_add_u64 v[150:151], s[2:3], 0, v[134:135]
	s_add_i32 m0, s46, 0x2000
	s_nop 0
	global_load_lds_dwordx4 v[150:151], off
	s_waitcnt vmcnt(6)
	s_setprio 1
	s_barrier
	v_mfma_f32_16x16x32_bf16 v[54:57], v[216:219], v[170:173], v[54:57]
	v_mfma_f32_16x16x32_bf16 v[50:53], v[224:227], v[170:173], v[50:53]
	v_mfma_f32_16x16x32_bf16 v[38:41], v[216:219], v[178:181], v[38:41]
	v_mfma_f32_16x16x32_bf16 v[34:37], v[224:227], v[178:181], v[34:37]
	v_mfma_f32_16x16x32_bf16 v[22:25], v[216:219], v[186:189], v[22:25]
	v_mfma_f32_16x16x32_bf16 v[18:21], v[224:227], v[186:189], v[18:21]
	v_mfma_f32_16x16x32_bf16 v[6:9], v[216:219], v[194:197], v[6:9]
	v_mfma_f32_16x16x32_bf16 v[2:5], v[224:227], v[194:197], v[2:5]
	v_mfma_f32_16x16x32_bf16 v[54:57], v[220:223], v[174:177], v[54:57]
	s_add_i32 s11, s11, 2
	v_mfma_f32_16x16x32_bf16 v[50:53], v[228:231], v[174:177], v[50:53]
	s_add_u32 s5, s5, 0x100
	v_mfma_f32_16x16x32_bf16 v[38:41], v[220:223], v[182:185], v[38:41]
	s_addc_u32 s9, s9, 0
	v_mfma_f32_16x16x32_bf16 v[34:37], v[228:231], v[182:185], v[34:37]
	s_cmp_gt_u32 s11, 13
	v_mfma_f32_16x16x32_bf16 v[22:25], v[220:223], v[190:193], v[22:25]
	s_mov_b64 s[2:3], s[36:37]
	v_mfma_f32_16x16x32_bf16 v[18:21], v[228:231], v[190:193], v[18:21]
	v_mfma_f32_16x16x32_bf16 v[6:9], v[220:223], v[198:201], v[6:9]
	v_mfma_f32_16x16x32_bf16 v[2:5], v[228:231], v[198:201], v[2:5]
	s_setprio 0
	s_barrier
	s_cbranch_scc0 .LBB0_320
	s_nop 0
	s_nop 0
	s_nop 0
	s_nop 0
	s_nop 0
	s_nop 0
	s_nop 0
	s_nop 0
	s_nop 0
	s_nop 0
	s_nop 0
	s_cmp_lt_i32 s14, 13
	s_cselect_b64 s[36:37], -1, 0
	s_and_b64 vcc, exec, s[36:37]
	s_cbranch_vccz .LBB0_325
	v_pk_mul_f32 v[154:155], v[126:127], v[126:127]
	v_pk_mul_f32 v[150:151], v[128:129], v[128:129]
	v_fmamk_f32 v0, v154, 0xbdd2d3e8, v202
	v_mul_f32_e32 v0, v126, v0
	v_exp_f32_e32 v154, v0
	v_fmamk_f32 v0, v155, 0xbdd2d3e8, v202
	v_mul_f32_e32 v0, v127, v0
	v_exp_f32_e32 v155, v0
	v_fmamk_f32 v0, v150, 0xbdd2d3e8, v202
	v_mul_f32_e32 v0, v128, v0
	v_exp_f32_e32 v150, v0
	v_fmamk_f32 v0, v151, 0xbdd2d3e8, v202
	v_mul_f32_e32 v0, v129, v0
	v_exp_f32_e32 v151, v0
	v_pk_add_f32 v[154:155], v[154:155], 1.0 op_sel_hi:[1,0]
	v_pk_add_f32 v[150:151], v[150:151], 1.0 op_sel_hi:[1,0]
	v_rcp_f32_e32 v154, v154
	v_rcp_f32_e32 v155, v155
	v_rcp_f32_e32 v150, v150
	v_rcp_f32_e32 v151, v151
	v_pk_mul_f32 v[126:127], v[126:127], v[154:155]
	v_pk_mul_f32 v[128:129], v[128:129], v[150:151]
	v_cndmask_b32_e64 v0, 0, 1, s[36:37]
	v_cmp_ne_u32_e64 s[2:3], 1, v0
	s_andn2_b64 vcc, exec, s[36:37]
	s_cbranch_vccz .LBB0_326

; #define G8_STAGE(bufoff, gbase, voff) do { _Pragma("unroll") for (int _i = 0; _i < 2; ++_i) \
;         __builtin_amdgcn_global_load_lds((const unsigned*)((const char*)(gbase) + (voff)[_i]), (LAS unsigned*)(lds + (bufoff) + ldsw + _i * 8192), 16, 0, 0); } while (0)
; #define G8_LDA(dst, b, h) do { _Pragma("unroll") for (int m = 0; m < 4; ++m) _Pragma("unroll") for (int k = 0; k < 2; ++k) dst[m][k] = *(const LAS bf16x8*)(lds + G8_SA(b, h) + aoff + m * 2048 + k * 1024); } while (0)
; #define G8_LDB(dst, b, h) do { _Pragma("unroll") for (int n = 0; n < 2; ++n) _Pragma("unroll") for (int k = 0; k < 2; ++k) dst[n][k] = *(const LAS bf16x8*)(lds + G8_SB(b, h) + boff + n * 2048 + k * 1024); } while (0)
; #define G8_MMA(ai, bj, At, Bt) do { __builtin_amdgcn_s_setprio(1); _Pragma("unroll") for (int m = 0; m < 4; ++m) _Pragma("unroll") for (int n = 0; n < 2; ++n) _Pragma("unroll") for (int k = 0; k < 2; ++k) \
;         acc[ai][bj][m][n] = __builtin_amdgcn_mfma_f32_16x16x32_bf16(Bt[n][k], At[m][k], acc[ai][bj][m][n], 0, 0, 0); __builtin_amdgcn_s_setprio(0); } while (0)
; #define G8_WAIT_L(n) asm volatile("s_waitcnt lgkmcnt(" #n ")" ::: "memory")
; #define G8_BAR __builtin_amdgcn_s_barrier()
; template <class Epi, class Sched>
; __device__ __forceinline__ void gemm_phase(LAS unsigned char* lds, const int K, const Sched& S, const Epi& E) {
;     ...
;         const bool has_next = S.next(ui + 1, nxt);
;         const char* nA = has_next ? nxt.A : cA; const char* nB = has_next ? nxt.B : cB;
; #pragma unroll 1
;         for (int t = 0; t < nt; t += 2) {
;             const bool last = (t == nt - 2);
;             const char* a1 = cA + (size_t)(t + 1) * kstep;
;             const char* a2 = last ? nA : cA + (size_t)(t + 2) * kstep; const char* b2 = last ? nB : cB + (size_t)(t + 2) * kstep;
;             const char* a3 = a2 + kstep; const char* b3 = b2 + kstep;
;             G8_LDB(B0, 0, 0); G8_SCHED; G8_LDA(At, 0, 0); G8_STAGE(G8_SA(1, 1), a1, oc[1]);
;             if (last && has_next) S.aoff(nxt, tid, oc);
;             G8_WAIT_L(8); G8_BAR; G8_WAIT_L(0); G8_MMA(0, 0, At, B0); G8_BAR; G8_SCHED;
;             G8_LDB(B1, 0, 1); G8_STAGE(G8_SB(0, 0), b2, voffB);
;             G8_BAR; G8_WAIT_L(0); G8_MMA(0, 1, At, B1); G8_BAR;
;             G8_LDA(At, 0, 1); G8_STAGE(G8_SA(0, 0), a2, oc[0]);
;             G8_BAR; G8_WAIT_L(0); G8_MMA(1, 0, At, B0); G8_BAR; G8_SCHED;
.LBB0_487:
	s_add_u32 s12, s0, 0x100
	s_addc_u32 s13, s1, 0
	s_add_i32 s49, 0, 0x10000
	v_add_u32_e32 v158, s49, v165
	ds_read_b128 v[130:133], v158
	ds_read_b128 v[134:137], v158 offset:1024
	ds_read_b128 v[154:157], v158 offset:2048
	ds_read_b128 v[158:161], v158 offset:3072
	s_cmp_eq_u32 s47, 12
	s_cselect_b32 s43, s23, s13
	s_cselect_b32 s42, s22, s12
	s_cselect_b32 s39, s37, s14
	s_cselect_b32 s38, s36, s3
	v_lshl_add_u64 v[162:163], s[0:1], 0, v[152:153]
	s_add_i32 m0, s76, 0xc000
	ds_read_b128 v[168:171], v167
	ds_read_b128 v[172:175], v167 offset:1024
	ds_read_b128 v[176:179], v167 offset:2048
	ds_read_b128 v[180:183], v167 offset:3072
	ds_read_b128 v[184:187], v167 offset:4096
	ds_read_b128 v[188:191], v167 offset:5120
	ds_read_b128 v[192:195], v167 offset:6144
	ds_read_b128 v[196:199], v167 offset:7168
	global_load_lds_dwordx4 v[162:163], off
	v_lshl_add_u64 v[162:163], s[0:1], 0, v[150:151]
	s_add_i32 m0, s76, 0xe000
	s_nop 0
	global_load_lds_dwordx4 v[162:163], off
	s_waitcnt lgkmcnt(8)
	s_setprio 1
	s_barrier
	s_waitcnt lgkmcnt(0)
	s_waitcnt lgkmcnt(0)
	v_mfma_f32_16x16x32_bf16 v[126:129], v[130:133], v[168:171], v[126:129]
	v_mfma_f32_16x16x32_bf16 v[118:121], v[154:157], v[168:171], v[118:121]
	v_mfma_f32_16x16x32_bf16 v[110:113], v[130:133], v[176:179], v[110:113]
	v_mfma_f32_16x16x32_bf16 v[102:105], v[154:157], v[176:179], v[102:105]
	v_mfma_f32_16x16x32_bf16 v[94:97], v[130:133], v[184:187], v[94:97]
	v_mfma_f32_16x16x32_bf16 v[86:89], v[154:157], v[184:187], v[86:89]
	v_mfma_f32_16x16x32_bf16 v[78:81], v[130:133], v[192:195], v[78:81]
	v_mfma_f32_16x16x32_bf16 v[70:73], v[154:157], v[192:195], v[70:73]
	v_mfma_f32_16x16x32_bf16 v[126:129], v[134:137], v[172:175], v[126:129]
	v_mfma_f32_16x16x32_bf16 v[118:121], v[158:161], v[172:175], v[118:121]
	v_mfma_f32_16x16x32_bf16 v[110:113], v[134:137], v[180:183], v[110:113]
	v_mfma_f32_16x16x32_bf16 v[102:105], v[158:161], v[180:183], v[102:105]
	v_mfma_f32_16x16x32_bf16 v[94:97], v[134:137], v[188:191], v[94:97]
	v_mfma_f32_16x16x32_bf16 v[86:89], v[158:161], v[188:191], v[86:89]
	v_mfma_f32_16x16x32_bf16 v[78:81], v[134:137], v[196:199], v[78:81]
	v_mfma_f32_16x16x32_bf16 v[70:73], v[158:161], v[196:199], v[70:73]
	s_setprio 0
	s_barrier
	s_add_i32 s54, 0, 0x14000
	v_add_u32_e32 v162, s54, v165
	s_add_i32 s0, s49, s65
	ds_read_b128 v[216:219], v162
	ds_read_b128 v[220:223], v162 offset:1024
	ds_read_b128 v[224:227], v162 offset:2048
	ds_read_b128 v[228:231], v162 offset:3072
	v_lshl_add_u64 v[162:163], s[38:39], 0, v[0:1]
	s_mov_b32 m0, s0
	v_lshl_add_u64 v[200:201], s[38:39], 0, v[140:141]
	global_load_lds_dwordx4 v[162:163], off
	s_add_i32 m0, s0, 0x2000
	s_nop 0
	global_load_lds_dwordx4 v[200:201], off
	s_setprio 1
	s_barrier
	s_waitcnt lgkmcnt(0)
	s_waitcnt lgkmcnt(0)
	v_mfma_f32_16x16x32_bf16 v[122:125], v[216:219], v[168:171], v[122:125]
	v_mfma_f32_16x16x32_bf16 v[114:117], v[224:227], v[168:171], v[114:117]
	v_mfma_f32_16x16x32_bf16 v[106:109], v[216:219], v[176:179], v[106:109]
	v_mfma_f32_16x16x32_bf16 v[98:101], v[224:227], v[176:179], v[98:101]
	v_mfma_f32_16x16x32_bf16 v[90:93], v[216:219], v[184:187], v[90:93]
	v_mfma_f32_16x16x32_bf16 v[82:85], v[224:227], v[184:187], v[82:85]
	v_mfma_f32_16x16x32_bf16 v[74:77], v[216:219], v[192:195], v[74:77]
	v_mfma_f32_16x16x32_bf16 v[66:69], v[224:227], v[192:195], v[66:69]
	v_mfma_f32_16x16x32_bf16 v[122:125], v[220:223], v[172:175], v[122:125]
	s_mov_b32 m0, s76
	v_mfma_f32_16x16x32_bf16 v[114:117], v[228:231], v[172:175], v[114:117]
	v_lshl_add_u64 v[232:233], s[42:43], 0, v[142:143]
	v_mfma_f32_16x16x32_bf16 v[106:109], v[220:223], v[180:183], v[106:109]
	v_mfma_f32_16x16x32_bf16 v[98:101], v[228:231], v[180:183], v[98:101]
	v_mfma_f32_16x16x32_bf16 v[90:93], v[220:223], v[188:191], v[90:93]
	v_mfma_f32_16x16x32_bf16 v[82:85], v[228:231], v[188:191], v[82:85]
	v_mfma_f32_16x16x32_bf16 v[74:77], v[220:223], v[196:199], v[74:77]
	v_mfma_f32_16x16x32_bf16 v[66:69], v[228:231], v[196:199], v[66:69]
	s_setprio 0
	s_barrier
	ds_read_b128 v[168:171], v167 offset:16384
	ds_read_b128 v[172:175], v167 offset:17408
	ds_read_b128 v[176:179], v167 offset:18432
	ds_read_b128 v[180:183], v167 offset:19456
	ds_read_b128 v[184:187], v167 offset:20480
	ds_read_b128 v[188:191], v167 offset:21504
	ds_read_b128 v[192:195], v167 offset:22528
	ds_read_b128 v[196:199], v167 offset:23552
	global_load_lds_dwordx4 v[232:233], off
	v_lshl_add_u64 v[234:235], s[42:43], 0, v[146:147]
	s_mov_b32 m0, s77
	s_nop 0
	global_load_lds_dwordx4 v[234:235], off
	s_setprio 1
	s_barrier
	s_waitcnt lgkmcnt(0)
	s_waitcnt lgkmcnt(0)
	v_mfma_f32_16x16x32_bf16 v[62:65], v[130:133], v[168:171], v[62:65]
	v_mfma_f32_16x16x32_bf16 v[54:57], v[154:157], v[168:171], v[54:57]
	v_mfma_f32_16x16x32_bf16 v[46:49], v[130:133], v[176:179], v[46:49]
	v_mfma_f32_16x16x32_bf16 v[38:41], v[154:157], v[176:179], v[38:41]
	v_mfma_f32_16x16x32_bf16 v[30:33], v[130:133], v[184:187], v[30:33]
	v_mfma_f32_16x16x32_bf16 v[22:25], v[154:157], v[184:187], v[22:25]
	v_mfma_f32_16x16x32_bf16 v[10:13], v[130:133], v[192:195], v[10:13]
	v_mfma_f32_16x16x32_bf16 v[2:5], v[154:157], v[192:195], v[2:5]
	v_mfma_f32_16x16x32_bf16 v[62:65], v[134:137], v[172:175], v[62:65]
	v_mfma_f32_16x16x32_bf16 v[54:57], v[158:161], v[172:175], v[54:57]
	v_mfma_f32_16x16x32_bf16 v[46:49], v[134:137], v[180:183], v[46:49]
	v_mfma_f32_16x16x32_bf16 v[38:41], v[158:161], v[180:183], v[38:41]
	v_mfma_f32_16x16x32_bf16 v[30:33], v[134:137], v[188:191], v[30:33]
	v_mfma_f32_16x16x32_bf16 v[22:25], v[158:161], v[188:191], v[22:25]
	v_mfma_f32_16x16x32_bf16 v[10:13], v[134:137], v[196:199], v[10:13]
	v_mfma_f32_16x16x32_bf16 v[2:5], v[158:161], v[196:199], v[2:5]
	s_setprio 0
	s_barrier
; #define G8_STAGE(bufoff, gbase, voff) do { _Pragma("unroll") for (int _i = 0; _i < 2; ++_i) \
;         __builtin_amdgcn_global_load_lds((const unsigned*)((const char*)(gbase) + (voff)[_i]), (LAS unsigned*)(lds + (bufoff) + ldsw + _i * 8192), 16, 0, 0); } while (0)
; #define G8_LDA(dst, b, h) do { _Pragma("unroll") for (int m = 0; m < 4; ++m) _Pragma("unroll") for (int k = 0; k < 2; ++k) dst[m][k] = *(const LAS bf16x8*)(lds + G8_SA(b, h) + aoff + m * 2048 + k * 1024); } while (0)
; #define G8_LDB(dst, b, h) do { _Pragma("unroll") for (int n = 0; n < 2; ++n) _Pragma("unroll") for (int k = 0; k < 2; ++k) dst[n][k] = *(const LAS bf16x8*)(lds + G8_SB(b, h) + boff + n * 2048 + k * 1024); } while (0)
; #define G8_MMA(ai, bj, At, Bt) do { __builtin_amdgcn_s_setprio(1); _Pragma("unroll") for (int m = 0; m < 4; ++m) _Pragma("unroll") for (int n = 0; n < 2; ++n) _Pragma("unroll") for (int k = 0; k < 2; ++k) \
;         acc[ai][bj][m][n] = __builtin_amdgcn_mfma_f32_16x16x32_bf16(Bt[n][k], At[m][k], acc[ai][bj][m][n], 0, 0, 0); __builtin_amdgcn_s_setprio(0); } while (0)
; #define G8_WAIT_V(n) asm volatile("s_waitcnt vmcnt(" #n ")" ::: "memory")
; #define G8_WAIT_L(n) asm volatile("s_waitcnt lgkmcnt(" #n ")" ::: "memory")
; #define G8_BAR __builtin_amdgcn_s_barrier()
; #define G8_SCHED __builtin_amdgcn_sched_barrier(0)
; template <class Epi, class Sched>
; __device__ __forceinline__ void gemm_phase(LAS unsigned char* lds, const int K, const Sched& S, const Epi& E) {
;     ...
;             G8_STAGE(G8_SB(0, 1), b2 + hstep, voffB);
;             G8_WAIT_V(6); G8_BAR; G8_MMA(1, 1, At, B1); G8_BAR;
;             G8_LDB(B0, 1, 0); G8_SCHED; G8_LDA(At, 1, 0); G8_STAGE(G8_SA(0, 1), a2, oc[1]);
;             G8_WAIT_L(8); G8_BAR; G8_WAIT_L(0); G8_MMA(0, 0, At, B0); G8_BAR; G8_SCHED;
;             G8_LDB(B1, 1, 1); G8_STAGE(G8_SB(1, 0), b3, voffB);
;             G8_BAR; G8_WAIT_L(0); G8_MMA(0, 1, At, B1); G8_BAR;
;             G8_LDA(At, 1, 1); G8_STAGE(G8_SA(1, 0), a3, oc[0]);
;             G8_BAR; G8_WAIT_L(0); G8_MMA(1, 0, At, B0); G8_BAR; G8_SCHED;
	s_add_u32 s0, s38, 0x40000
	s_addc_u32 s1, s39, 0
	s_add_i32 s49, s54, s65
	v_lshl_add_u64 v[130:131], s[0:1], 0, v[0:1]
	s_mov_b32 m0, s49
	s_nop 0
	global_load_lds_dwordx4 v[130:131], off
	v_lshl_add_u64 v[130:131], s[0:1], 0, v[140:141]
	s_add_i32 m0, s49, 0x2000
	s_nop 0
	global_load_lds_dwordx4 v[130:131], off
	s_waitcnt vmcnt(6)
	s_setprio 1
	s_barrier
	v_mfma_f32_16x16x32_bf16 v[58:61], v[216:219], v[168:171], v[58:61]
	v_mfma_f32_16x16x32_bf16 v[50:53], v[224:227], v[168:171], v[50:53]
	v_mfma_f32_16x16x32_bf16 v[42:45], v[216:219], v[176:179], v[42:45]
	v_mfma_f32_16x16x32_bf16 v[34:37], v[224:227], v[176:179], v[34:37]
	v_mfma_f32_16x16x32_bf16 v[26:29], v[216:219], v[184:187], v[26:29]
	v_mfma_f32_16x16x32_bf16 v[18:21], v[224:227], v[184:187], v[18:21]
	v_mfma_f32_16x16x32_bf16 v[14:17], v[216:219], v[192:195], v[14:17]
	v_mfma_f32_16x16x32_bf16 v[6:9], v[224:227], v[192:195], v[6:9]
	v_mfma_f32_16x16x32_bf16 v[58:61], v[220:223], v[172:175], v[58:61]
	s_add_i32 s0, 0, 0x18000
	v_mfma_f32_16x16x32_bf16 v[50:53], v[228:231], v[172:175], v[50:53]
	v_add_u32_e32 v158, s0, v165
	v_mfma_f32_16x16x32_bf16 v[42:45], v[220:223], v[180:183], v[42:45]
	v_mfma_f32_16x16x32_bf16 v[34:37], v[228:231], v[180:183], v[34:37]
	v_mfma_f32_16x16x32_bf16 v[26:29], v[220:223], v[188:191], v[26:29]
	v_mfma_f32_16x16x32_bf16 v[18:21], v[228:231], v[188:191], v[18:21]
	v_mfma_f32_16x16x32_bf16 v[14:17], v[220:223], v[196:199], v[14:17]
	v_mfma_f32_16x16x32_bf16 v[6:9], v[228:231], v[196:199], v[6:9]
	s_setprio 0
	s_barrier
	ds_read_b128 v[130:133], v158
	ds_read_b128 v[134:137], v158 offset:1024
	ds_read_b128 v[154:157], v158 offset:2048
	ds_read_b128 v[158:161], v158 offset:3072
	s_mov_b32 m0, s78
	v_lshl_add_u64 v[216:217], s[42:43], 0, v[144:145]
	ds_read_b128 v[168:171], v167 offset:32768
	ds_read_b128 v[172:175], v167 offset:33792
	ds_read_b128 v[176:179], v167 offset:34816
	ds_read_b128 v[180:183], v167 offset:35840
	ds_read_b128 v[184:187], v167 offset:36864
	ds_read_b128 v[188:191], v167 offset:37888
	ds_read_b128 v[192:195], v167 offset:38912
	ds_read_b128 v[196:199], v167 offset:39936
	global_load_lds_dwordx4 v[216:217], off
	v_lshl_add_u64 v[216:217], s[42:43], 0, v[148:149]
	s_mov_b32 m0, s79
	s_nop 0
	global_load_lds_dwordx4 v[216:217], off
	s_waitcnt lgkmcnt(8)
	s_setprio 1
	s_barrier
	s_waitcnt lgkmcnt(0)
	s_waitcnt lgkmcnt(0)
	v_mfma_f32_16x16x32_bf16 v[126:129], v[130:133], v[168:171], v[126:129]
	v_mfma_f32_16x16x32_bf16 v[118:121], v[154:157], v[168:171], v[118:121]
	v_mfma_f32_16x16x32_bf16 v[110:113], v[130:133], v[176:179], v[110:113]
	v_mfma_f32_16x16x32_bf16 v[102:105], v[154:157], v[176:179], v[102:105]
	v_mfma_f32_16x16x32_bf16 v[94:97], v[130:133], v[184:187], v[94:97]
	v_mfma_f32_16x16x32_bf16 v[86:89], v[154:157], v[184:187], v[86:89]
	v_mfma_f32_16x16x32_bf16 v[78:81], v[130:133], v[192:195], v[78:81]
	v_mfma_f32_16x16x32_bf16 v[70:73], v[154:157], v[192:195], v[70:73]
	v_mfma_f32_16x16x32_bf16 v[126:129], v[134:137], v[172:175], v[126:129]
	v_mfma_f32_16x16x32_bf16 v[118:121], v[158:161], v[172:175], v[118:121]
	v_mfma_f32_16x16x32_bf16 v[110:113], v[134:137], v[180:183], v[110:113]
	v_mfma_f32_16x16x32_bf16 v[102:105], v[158:161], v[180:183], v[102:105]
	v_mfma_f32_16x16x32_bf16 v[94:97], v[134:137], v[188:191], v[94:97]
	v_mfma_f32_16x16x32_bf16 v[86:89], v[158:161], v[188:191], v[86:89]
	v_mfma_f32_16x16x32_bf16 v[78:81], v[134:137], v[196:199], v[78:81]
	v_mfma_f32_16x16x32_bf16 v[70:73], v[158:161], v[196:199], v[70:73]
	s_setprio 0
	s_barrier
	s_add_i32 s42, 0, 0x1c000
	s_add_i32 s0, s0, s65
	v_add_u32_e32 v213, s42, v165
	v_lshl_add_u64 v[162:163], v[162:163], 0, s[18:19]
	s_mov_b32 m0, s0
	ds_read_b128 v[216:219], v213
	ds_read_b128 v[220:223], v213 offset:1024
	ds_read_b128 v[224:227], v213 offset:2048
	ds_read_b128 v[228:231], v213 offset:3072
	global_load_lds_dwordx4 v[162:163], off
	v_lshl_add_u64 v[162:163], v[200:201], 0, s[18:19]
	s_add_i32 m0, s0, 0x2000
	s_nop 0
	global_load_lds_dwordx4 v[162:163], off
	s_setprio 1
	s_barrier
	s_waitcnt lgkmcnt(0)
	s_waitcnt lgkmcnt(0)
	v_mfma_f32_16x16x32_bf16 v[122:125], v[216:219], v[168:171], v[122:125]
	v_mfma_f32_16x16x32_bf16 v[114:117], v[224:227], v[168:171], v[114:117]
	v_mfma_f32_16x16x32_bf16 v[106:109], v[216:219], v[176:179], v[106:109]
	v_mfma_f32_16x16x32_bf16 v[98:101], v[224:227], v[176:179], v[98:101]
	v_mfma_f32_16x16x32_bf16 v[90:93], v[216:219], v[184:187], v[90:93]
	v_mfma_f32_16x16x32_bf16 v[82:85], v[224:227], v[184:187], v[82:85]
	v_mfma_f32_16x16x32_bf16 v[74:77], v[216:219], v[192:195], v[74:77]
	v_mfma_f32_16x16x32_bf16 v[66:69], v[224:227], v[192:195], v[66:69]
	v_mfma_f32_16x16x32_bf16 v[122:125], v[220:223], v[172:175], v[122:125]
	s_mov_b32 m0, s81
	v_mfma_f32_16x16x32_bf16 v[114:117], v[228:231], v[172:175], v[114:117]
	v_lshl_add_u64 v[162:163], v[232:233], 0, s[18:19]
	v_mfma_f32_16x16x32_bf16 v[106:109], v[220:223], v[180:183], v[106:109]
	v_mfma_f32_16x16x32_bf16 v[98:101], v[228:231], v[180:183], v[98:101]
	v_mfma_f32_16x16x32_bf16 v[90:93], v[220:223], v[188:191], v[90:93]
	v_mfma_f32_16x16x32_bf16 v[82:85], v[228:231], v[188:191], v[82:85]
	v_mfma_f32_16x16x32_bf16 v[74:77], v[220:223], v[196:199], v[74:77]
	v_mfma_f32_16x16x32_bf16 v[66:69], v[228:231], v[196:199], v[66:69]
	s_setprio 0
	s_barrier
	ds_read_b128 v[168:171], v167 offset:49152
	ds_read_b128 v[172:175], v167 offset:50176
	ds_read_b128 v[176:179], v167 offset:51200
	ds_read_b128 v[180:183], v167 offset:52224
	ds_read_b128 v[184:187], v167 offset:53248
	ds_read_b128 v[188:191], v167 offset:54272
	ds_read_b128 v[192:195], v167 offset:55296
	ds_read_b128 v[196:199], v167 offset:56320
	global_load_lds_dwordx4 v[162:163], off
	v_lshl_add_u64 v[162:163], v[234:235], 0, s[18:19]
	s_mov_b32 m0, s82
	s_nop 0
	global_load_lds_dwordx4 v[162:163], off
	s_setprio 1
	s_barrier
; #define G8_WAIT_V(n) asm volatile("s_waitcnt vmcnt(" #n ")" ::: "memory")
; #define G8_WAIT_L(n) asm volatile("s_waitcnt lgkmcnt(" #n ")" ::: "memory")
; template <class Epi, class Sched>
; __device__ __forceinline__ void gemm_phase(LAS unsigned char* lds, const int K, const Sched& S, const Epi& E) {
;     ...
;             G8_BAR; G8_WAIT_L(0); G8_MMA(1, 0, At, B0); G8_BAR; G8_SCHED;
;             G8_STAGE(G8_SB(1, 1), b3 + hstep, voffB);
;             G8_WAIT_V(6); G8_BAR; G8_MMA(1, 1, At, B1); G8_BAR;
;         }
;     __device__ __forceinline__ void operator()(const f32x4 (&acc)[2][2][4][2], const g8::Unit& u, int wr, int wc, int fr_, int fq_) const {
;     ...
;         const int pn = u.pn; const int colp = pn * 256 + wc * 32 + fq * 8;
;         bf16_t* qb = (bf16_t*)(ws + AB_QB); bf16_t* kb = (bf16_t*)(ws + AB_KB); bf16_t* vT = (bf16_t*)(ws + AB_VT); bf16_t* rqb = (bf16_t*)(ws + AB_RQB); bf16_t* rkb = (bf16_t*)(ws + AB_RKB);
;         bf16_t* rkdT = (bf16_t*)(ws + AB_RKDT); bf16_t* rvT = (bf16_t*)(ws + AB_RVT); bf16_t* rgb = (bf16_t*)(ws + AB_RGB);
;         const float frqA0 = exp2f(-(float)(fq * 8) * (13.287712379549449f / 32.f)) * 0.15915494309189535f;
;         const float frqR0 = exp2f(-(float)((wc & 1) * 32 + fq * 8) * (13.287712379549449f / 63.f)) * 0.15915494309189535f;
;         constexpr float RA[8] = {1.f, 0.7498942093324559f, 0.5623413251903491f, 0.4216965034285822f, 0.31622776601683794f, 0.23713737056616552f, 0.1778279410038923f, 0.1333521432163324f};
;         constexpr float RR[8] = {1.f, 0.8639884494839686f, 0.746476040841712f, 0.6449466771037624f, 0.5572264795507174f, 0.4814372420784346f, 0.4159562163071847f, 0.35938136638046275f};
; #pragma unroll
;         for (int ai = 0; ai < 2; ++ai)
; #pragma unroll
;             for (int m = 0; m < 4; ++m) {
;                 const int t = u.pm * 256 + ai * 128 + wr * 64 + m * 16 + fr, sq = t & (SEQ - 1), b = t >> 13;
;                 f32x4 x[2][2];
; #pragma unroll
;                 for (int bj = 0; bj < 2; ++bj)
; #pragma unroll
;                     for (int n = 0; n < 2; ++n) x[bj][n] = acc[ai][bj][m][n];
;                 if (pn < 4 || (pn == 4 && wc < 2)) {
;                     const int j0 = fq * 8; const float sc = pn < 4 ? 0.125f : 1.f;
;                     u32x4 w1, w2;
; #pragma unroll
;                     for (int n = 0; n < 2; ++n) { f32x4 o1, o2;
; #pragma unroll
	s_waitcnt lgkmcnt(0)
	s_waitcnt lgkmcnt(0)
	v_mfma_f32_16x16x32_bf16 v[62:65], v[130:133], v[168:171], v[62:65]
	v_mfma_f32_16x16x32_bf16 v[54:57], v[154:157], v[168:171], v[54:57]
	v_mfma_f32_16x16x32_bf16 v[46:49], v[130:133], v[176:179], v[46:49]
	v_mfma_f32_16x16x32_bf16 v[38:41], v[154:157], v[176:179], v[38:41]
	v_mfma_f32_16x16x32_bf16 v[30:33], v[130:133], v[184:187], v[30:33]
	v_mfma_f32_16x16x32_bf16 v[22:25], v[154:157], v[184:187], v[22:25]
	v_mfma_f32_16x16x32_bf16 v[10:13], v[130:133], v[192:195], v[10:13]
	v_mfma_f32_16x16x32_bf16 v[2:5], v[154:157], v[192:195], v[2:5]
	v_mfma_f32_16x16x32_bf16 v[62:65], v[134:137], v[172:175], v[62:65]
	v_mfma_f32_16x16x32_bf16 v[54:57], v[158:161], v[172:175], v[54:57]
	v_mfma_f32_16x16x32_bf16 v[46:49], v[134:137], v[180:183], v[46:49]
	v_mfma_f32_16x16x32_bf16 v[38:41], v[158:161], v[180:183], v[38:41]
	v_mfma_f32_16x16x32_bf16 v[30:33], v[134:137], v[188:191], v[30:33]
	v_mfma_f32_16x16x32_bf16 v[22:25], v[158:161], v[188:191], v[22:25]
	v_mfma_f32_16x16x32_bf16 v[10:13], v[134:137], v[196:199], v[10:13]
	v_mfma_f32_16x16x32_bf16 v[2:5], v[158:161], v[196:199], v[2:5]
	s_setprio 0
	s_barrier
	s_add_u32 s0, s38, 0x40080
	s_addc_u32 s1, s39, 0
	s_add_i32 s38, s42, s65
	v_lshl_add_u64 v[130:131], s[0:1], 0, v[0:1]
	s_mov_b32 m0, s38
	s_nop 0
	global_load_lds_dwordx4 v[130:131], off
	v_lshl_add_u64 v[130:131], s[0:1], 0, v[140:141]
	s_add_i32 m0, s38, 0x2000
	s_nop 0
	global_load_lds_dwordx4 v[130:131], off
	s_waitcnt vmcnt(6)
	s_setprio 1
	s_barrier
	v_mfma_f32_16x16x32_bf16 v[58:61], v[216:219], v[168:171], v[58:61]
	v_mfma_f32_16x16x32_bf16 v[50:53], v[224:227], v[168:171], v[50:53]
	v_mfma_f32_16x16x32_bf16 v[42:45], v[216:219], v[176:179], v[42:45]
	v_mfma_f32_16x16x32_bf16 v[34:37], v[224:227], v[176:179], v[34:37]
	v_mfma_f32_16x16x32_bf16 v[26:29], v[216:219], v[184:187], v[26:29]
	v_mfma_f32_16x16x32_bf16 v[18:21], v[224:227], v[184:187], v[18:21]
	v_mfma_f32_16x16x32_bf16 v[14:17], v[216:219], v[192:195], v[14:17]
	v_mfma_f32_16x16x32_bf16 v[6:9], v[224:227], v[192:195], v[6:9]
	v_mfma_f32_16x16x32_bf16 v[58:61], v[220:223], v[172:175], v[58:61]
	s_add_i32 s47, s47, 2
	v_mfma_f32_16x16x32_bf16 v[50:53], v[228:231], v[172:175], v[50:53]
	s_add_u32 s3, s3, 0x100
	v_mfma_f32_16x16x32_bf16 v[42:45], v[220:223], v[180:183], v[42:45]
	s_addc_u32 s14, s14, 0
	v_mfma_f32_16x16x32_bf16 v[34:37], v[228:231], v[180:183], v[34:37]
	s_cmp_gt_u32 s47, 13
	v_mfma_f32_16x16x32_bf16 v[26:29], v[220:223], v[188:191], v[26:29]
	s_mov_b64 s[0:1], s[12:13]
	v_mfma_f32_16x16x32_bf16 v[18:21], v[228:231], v[188:191], v[18:21]
	v_mfma_f32_16x16x32_bf16 v[14:17], v[220:223], v[196:199], v[14:17]
	v_mfma_f32_16x16x32_bf16 v[6:9], v[228:231], v[196:199], v[6:9]
	s_setprio 0
	s_barrier
	s_cbranch_scc0 .LBB0_487
	s_nop 0
	s_nop 0
	s_nop 0
	s_nop 0
	s_nop 0
	s_nop 0
	s_nop 0
	s_nop 0
	s_nop 0
	s_nop 0
	s_lshl_b32 s2, s2, 8
	s_add_i32 s2, s2, s80
	s_cmp_lt_i32 s94, 4
	s_cselect_b64 s[36:37], -1, 0
	s_cmp_lg_u32 s94, 4
	v_mov_b32_e32 v131, v164
	v_mov_b32_e32 v130, v139
	s_cselect_b64 s[12:13], -1, 0
	s_cmp_eq_u32 s94, 4
	s_nop 0
	v_add_u32_e32 v160, s2, v131
	s_cselect_b64 s[2:3], -1, 0
	s_and_b64 s[2:3], s[2:3], s[10:11]
	s_cmp_gt_u32 s94, 8
	s_cselect_b64 s[56:57], -1, 0
	s_cmp_gt_u32 s94, 12
	s_cselect_b64 s[54:55], -1, 0
	s_lshl_b32 s42, s94, 8
	s_add_i32 s14, s42, 0xfffff300
	v_lshlrev_b32_e32 v130, 3, v130
	s_lshl_b64 s[22:23], s[14:15], 1
	v_add_u32_e32 v132, s85, v130
	s_add_u32 s22, s87, s22
	v_cvt_f32_i32_e32 v133, v132
	s_addc_u32 s23, s88, s23
	s_add_i32 s14, s86, s42
	s_cmp_gt_u32 s94, 6
	v_add_u32_e32 v171, s14, v130
	s_cselect_b64 s[38:39], -1, 0
	s_lshl_b32 s14, s94, 1
	s_and_b32 s14, s14, 2
	v_mul_f32_e32 v134, 0xbe57fa62, v133
	s_or_b32 s14, s14, s89
	v_cmp_gt_f32_e32 vcc, s66, v134
	v_ashrrev_i32_e32 v131, 31, v130
	s_lshl_b32 s14, s14, 7
	v_cvt_f32_i32_e32 v172, v130
	v_cndmask_b32_e32 v134, 0, v207, vcc
	v_lshlrev_b64 v[162:163], 1, v[130:131]
	s_xor_b32 s14, s14, 0x100
	v_fmac_f32_e32 v134, 0xbe57fa62, v133
	v_lshl_add_u64 v[158:159], s[22:23], 0, v[162:163]
	s_and_b64 s[22:23], s[38:39], exec
	v_exp_f32_e32 v133, v134
	s_mov_b32 s22, 0x3d420000
	s_cselect_b32 s22, s22, 0x3c420000
	v_mul_f32_e32 v134, 0xbed49a78, v172
	s_add_u32 s22, s40, s22
	v_cmp_gt_f32_e64 s[0:1], s66, v134
	v_cndmask_b32_e32 v134, 0, v208, vcc
	v_add_u32_e32 v170, s14, v132
	s_addc_u32 s23, s41, 0
	s_lshl_b32 s14, s14, 1
	v_ldexp_f32 v133, v133, v134
	s_add_u32 s22, s22, s14
	v_mul_f32_e32 v169, 0.15915494, v133
	s_addc_u32 s23, s23, 0
	v_ashrrev_i32_e32 v133, 31, v132
	v_lshl_add_u64 v[154:155], v[132:133], 1, s[22:23]
	s_or_b32 s22, s42, s75
	s_ashr_i32 s23, s22, 31
	s_lshl_b64 s[22:23], s[22:23], 1
	s_add_u32 s42, s83, s22
	v_mov_b32_e32 v131, 0x3db504f3
	s_addc_u32 s43, s84, s23
	s_nor_b64 s[22:23], s[36:37], s[2:3]
	v_cndmask_b32_e64 v156, 1.0, v131, s[38:39]
	v_add_u32_e32 v168, s90, v130
	v_and_b32_e32 v173, 0x1fff, v160
	s_mov_b64 s[2:3], -1
	s_and_b64 vcc, exec, s[22:23]
	s_cbranch_vccz .LBB0_506
; __device__ __forceinline__ unsigned pk2(float lo, float hi) { unsigned r; asm("v_cvt_pk_bf16_f32 %0, %1, %2" : "=v"(r) : "v"(lo), "v"(hi)); return r; }
; __device__ __forceinline__ f32x4 silu4(const f32x4 x) { const f32x4 t = x * (-1.4426950408889634f); f32x4 d;
; #pragma unroll
;     for (int e = 0; e < 4; ++e) d[e] = __builtin_amdgcn_exp2f(t[e]);
;     d = d + 1.f;
; #pragma unroll
;     for (int e = 0; e < 4; ++e) d[e] = __builtin_amdgcn_rcpf(d[e]);
;     return x * d; }
;     __device__ __forceinline__ void operator()(const f32x4 (&acc)[2][2][4][2], const g8::Unit& u, int wr, int wc, int fr_, int fq_) const {
;     ...
;                 } else {
; #pragma unroll
;                     for (int bj = 0; bj < 2; ++bj) { u32x4 w;
; #pragma unroll
;                         for (int n = 0; n < 2; ++n) { const f32x4 sv = silu4(x[bj][n]); w[2 * n] = pk2(sv[0], sv[1]); w[2 * n + 1] = pk2(sv[2], sv[3]); }
;                         *(u32x4*)(rgb + (size_t)t * 1024 + (pn - 13) * 256 + bj * 128 + wc * 32 + fq * 8) = w; }
	v_ashrrev_i32_e32 v174, 13, v160
	s_and_b64 vcc, exec, s[12:13]
	s_cbranch_vccz .LBB0_503
	s_and_b64 vcc, exec, s[56:57]
	s_cbranch_vccz .LBB0_496
	s_andn2_b64 vcc, exec, s[54:55]
	s_cbranch_vccnz .LBB0_493
	v_mul_f32_e32 v132, 0xbfb8aa3b, v126
	v_mul_f32_e32 v133, 0xbfb8aa3b, v127
	v_mul_f32_e32 v134, 0xbfb8aa3b, v128
	v_mul_f32_e32 v135, 0xbfb8aa3b, v129
	v_exp_f32_e32 v132, v132
	v_exp_f32_e32 v133, v133
	v_exp_f32_e32 v134, v134
	v_exp_f32_e32 v135, v135
	v_mul_f32_e32 v136, 0xbfb8aa3b, v120
	v_pk_add_f32 v[132:133], v[132:133], 1.0 op_sel_hi:[1,0]
	v_mul_f32_e32 v137, 0xbfb8aa3b, v121
	v_pk_add_f32 v[134:135], v[134:135], 1.0 op_sel_hi:[1,0]
	v_rcp_f32_e32 v132, v132
	v_rcp_f32_e32 v133, v133
	v_rcp_f32_e32 v134, v134
	v_rcp_f32_e32 v135, v135
	v_exp_f32_e32 v136, v136
	v_pk_mul_f32 v[132:133], v[126:127], v[132:133]
	v_exp_f32_e32 v137, v137
	v_pk_mul_f32 v[134:135], v[128:129], v[134:135]
	v_cvt_pk_bf16_f32 v132, v132, v133
	v_ashrrev_i32_e32 v161, 31, v160
	v_cvt_pk_bf16_f32 v133, v134, v135
	v_mul_f32_e32 v134, 0xbfb8aa3b, v118
	v_mul_f32_e32 v135, 0xbfb8aa3b, v119
	v_exp_f32_e32 v134, v134
	v_exp_f32_e32 v135, v135
	v_pk_add_f32 v[136:137], v[136:137], 1.0 op_sel_hi:[1,0]
	v_lshlrev_b64 v[130:131], 11, v[160:161]
	v_rcp_f32_e32 v136, v136
	v_pk_add_f32 v[134:135], v[134:135], 1.0 op_sel_hi:[1,0]
	v_rcp_f32_e32 v137, v137
	v_rcp_f32_e32 v134, v134
	v_rcp_f32_e32 v135, v135
	v_lshl_add_u64 v[130:131], v[158:159], 0, v[130:131]
	v_pk_mul_f32 v[136:137], v[120:121], v[136:137]
	s_mov_b64 s[2:3], 0
	v_pk_mul_f32 v[134:135], v[118:119], v[134:135]
	s_nop 0
	v_cvt_pk_bf16_f32 v134, v134, v135
	v_cvt_pk_bf16_f32 v135, v136, v137
	global_store_dwordx4 v[130:131], v[132:135], off
	v_mul_f32_e32 v136, 0xbfb8aa3b, v116
	v_mul_f32_e32 v137, 0xbfb8aa3b, v117
	v_mul_f32_e32 v132, 0xbfb8aa3b, v122
	v_mul_f32_e32 v133, 0xbfb8aa3b, v123
	v_mul_f32_e32 v134, 0xbfb8aa3b, v124
	v_mul_f32_e32 v135, 0xbfb8aa3b, v125
	v_exp_f32_e32 v132, v132
	v_exp_f32_e32 v133, v133
	v_exp_f32_e32 v134, v134
	v_exp_f32_e32 v135, v135
	v_exp_f32_e32 v136, v136
	v_pk_add_f32 v[132:133], v[132:133], 1.0 op_sel_hi:[1,0]
	v_exp_f32_e32 v137, v137
	v_pk_add_f32 v[134:135], v[134:135], 1.0 op_sel_hi:[1,0]
	v_rcp_f32_e32 v132, v132
	v_rcp_f32_e32 v133, v133
	v_rcp_f32_e32 v134, v134
	v_rcp_f32_e32 v135, v135
	v_pk_add_f32 v[136:137], v[136:137], 1.0 op_sel_hi:[1,0]
	v_pk_mul_f32 v[132:133], v[122:123], v[132:133]
	v_rcp_f32_e32 v136, v136
	v_pk_mul_f32 v[134:135], v[124:125], v[134:135]
	v_cvt_pk_bf16_f32 v132, v132, v133
	v_rcp_f32_e32 v137, v137
	v_cvt_pk_bf16_f32 v133, v134, v135
	v_mul_f32_e32 v134, 0xbfb8aa3b, v114
	v_mul_f32_e32 v135, 0xbfb8aa3b, v115
	v_exp_f32_e32 v134, v134
	v_exp_f32_e32 v135, v135
	v_pk_mul_f32 v[136:137], v[116:117], v[136:137]
	v_pk_add_f32 v[134:135], v[134:135], 1.0 op_sel_hi:[1,0]
	s_nop 0
	v_rcp_f32_e32 v134, v134
	v_rcp_f32_e32 v135, v135
	s_nop 0
	v_pk_mul_f32 v[134:135], v[114:115], v[134:135]
	s_nop 0
	v_cvt_pk_bf16_f32 v134, v134, v135
	v_cvt_pk_bf16_f32 v135, v136, v137
	global_store_dwordx4 v[130:131], v[132:135], off offset:256

; #define G8_STAGE(bufoff, gbase, voff) do { _Pragma("unroll") for (int _i = 0; _i < 2; ++_i) \
;         __builtin_amdgcn_global_load_lds((const unsigned*)((const char*)(gbase) + (voff)[_i]), (LAS unsigned*)(lds + (bufoff) + ldsw + _i * 8192), 16, 0, 0); } while (0)
; #define G8_LDA(dst, b, h) do { _Pragma("unroll") for (int m = 0; m < 4; ++m) _Pragma("unroll") for (int k = 0; k < 2; ++k) dst[m][k] = *(const LAS bf16x8*)(lds + G8_SA(b, h) + aoff + m * 2048 + k * 1024); } while (0)
; #define G8_LDB(dst, b, h) do { _Pragma("unroll") for (int n = 0; n < 2; ++n) _Pragma("unroll") for (int k = 0; k < 2; ++k) dst[n][k] = *(const LAS bf16x8*)(lds + G8_SB(b, h) + boff + n * 2048 + k * 1024); } while (0)
; #define G8_MMA(ai, bj, At, Bt) do { __builtin_amdgcn_s_setprio(1); _Pragma("unroll") for (int m = 0; m < 4; ++m) _Pragma("unroll") for (int n = 0; n < 2; ++n) _Pragma("unroll") for (int k = 0; k < 2; ++k) \
;         acc[ai][bj][m][n] = __builtin_amdgcn_mfma_f32_16x16x32_bf16(Bt[n][k], At[m][k], acc[ai][bj][m][n], 0, 0, 0); __builtin_amdgcn_s_setprio(0); } while (0)
; #define G8_WAIT_L(n) asm volatile("s_waitcnt lgkmcnt(" #n ")" ::: "memory")
; #define G8_BAR __builtin_amdgcn_s_barrier()
; template <class Epi, class Sched>
; __device__ __forceinline__ void gemm_phase(LAS unsigned char* lds, const int K, const Sched& S, const Epi& E) {
;     ...
;         const bool has_next = S.next(ui + 1, nxt);
;         const char* nA = has_next ? nxt.A : cA; const char* nB = has_next ? nxt.B : cB;
; #pragma unroll 1
;         for (int t = 0; t < nt; t += 2) {
;             const bool last = (t == nt - 2);
;             const char* a1 = cA + (size_t)(t + 1) * kstep;
;             const char* a2 = last ? nA : cA + (size_t)(t + 2) * kstep; const char* b2 = last ? nB : cB + (size_t)(t + 2) * kstep;
;             const char* a3 = a2 + kstep; const char* b3 = b2 + kstep;
;             G8_LDB(B0, 0, 0); G8_SCHED; G8_LDA(At, 0, 0); G8_STAGE(G8_SA(1, 1), a1, oc[1]);
;             if (last && has_next) S.aoff(nxt, tid, oc);
;             G8_WAIT_L(8); G8_BAR; G8_WAIT_L(0); G8_MMA(0, 0, At, B0); G8_BAR; G8_SCHED;
;             G8_LDB(B1, 0, 1); G8_STAGE(G8_SB(0, 0), b2, voffB);
;             G8_BAR; G8_WAIT_L(0); G8_MMA(0, 1, At, B1); G8_BAR;
;             G8_LDA(At, 0, 1); G8_STAGE(G8_SA(0, 0), a2, oc[0]);
;             G8_BAR; G8_WAIT_L(0); G8_MMA(1, 0, At, B0); G8_BAR; G8_SCHED;
.LBB0_2252:
	s_add_i32 s60, s22, 2
	s_add_u32 s24, s12, 0x80
	s_addc_u32 s23, s13, 0
	s_add_i32 s61, 0, 0x10000
	v_add_u32_e32 v144, s61, v148
	ds_read_b128 v[152:155], v144
	ds_read_b128 v[156:159], v144 offset:1024
	ds_read_b128 v[160:163], v144 offset:2048
	ds_read_b128 v[164:167], v144 offset:3072
	s_cmp_eq_u32 s51, s22
	s_cselect_b32 s22, s0, s24
	s_cselect_b32 s23, s1, s23
	s_cselect_b32 s25, s11, s59
	s_cselect_b32 s24, s10, s58
	v_lshl_add_u64 v[144:145], s[12:13], 0, v[140:141]
	s_add_i32 m0, s44, 0xc000
	ds_read_b128 v[168:171], v150
	ds_read_b128 v[172:175], v150 offset:1024
	ds_read_b128 v[176:179], v150 offset:2048
	ds_read_b128 v[180:183], v150 offset:3072
	ds_read_b128 v[184:187], v150 offset:4096
	ds_read_b128 v[188:191], v150 offset:5120
	ds_read_b128 v[192:195], v150 offset:6144
	ds_read_b128 v[196:199], v150 offset:7168
	global_load_lds_dwordx4 v[144:145], off
	v_lshl_add_u64 v[144:145], s[12:13], 0, v[142:143]
	s_add_i32 m0, s44, 0xe000
	s_nop 0
	global_load_lds_dwordx4 v[144:145], off
	s_waitcnt lgkmcnt(8)
	s_setprio 1
	s_barrier
	s_waitcnt lgkmcnt(0)
	s_waitcnt lgkmcnt(0)
	v_mfma_f32_16x16x32_bf16 v[126:129], v[152:155], v[168:171], v[126:129]
	v_mfma_f32_16x16x32_bf16 v[122:125], v[160:163], v[168:171], v[122:125]
	v_mfma_f32_16x16x32_bf16 v[110:113], v[152:155], v[176:179], v[110:113]
	v_mfma_f32_16x16x32_bf16 v[106:109], v[160:163], v[176:179], v[106:109]
	v_mfma_f32_16x16x32_bf16 v[94:97], v[152:155], v[184:187], v[94:97]
	v_mfma_f32_16x16x32_bf16 v[90:93], v[160:163], v[184:187], v[90:93]
	v_mfma_f32_16x16x32_bf16 v[78:81], v[152:155], v[192:195], v[78:81]
	v_mfma_f32_16x16x32_bf16 v[74:77], v[160:163], v[192:195], v[74:77]
	v_mfma_f32_16x16x32_bf16 v[126:129], v[156:159], v[172:175], v[126:129]
	v_mfma_f32_16x16x32_bf16 v[122:125], v[164:167], v[172:175], v[122:125]
	v_mfma_f32_16x16x32_bf16 v[110:113], v[156:159], v[180:183], v[110:113]
	v_mfma_f32_16x16x32_bf16 v[106:109], v[164:167], v[180:183], v[106:109]
	v_mfma_f32_16x16x32_bf16 v[94:97], v[156:159], v[188:191], v[94:97]
	v_mfma_f32_16x16x32_bf16 v[90:93], v[164:167], v[188:191], v[90:93]
	v_mfma_f32_16x16x32_bf16 v[78:81], v[156:159], v[196:199], v[78:81]
	v_mfma_f32_16x16x32_bf16 v[74:77], v[164:167], v[196:199], v[74:77]
	s_setprio 0
	s_barrier
	s_add_i32 s62, 0, 0x14000
	v_add_u32_e32 v144, s62, v148
	s_add_i32 s61, s61, s43
	ds_read_b128 v[216:219], v144
	ds_read_b128 v[220:223], v144 offset:1024
	ds_read_b128 v[224:227], v144 offset:2048
	ds_read_b128 v[228:231], v144 offset:3072
	v_lshl_add_u64 v[144:145], s[24:25], 0, v[0:1]
	s_mov_b32 m0, s61
	v_lshl_add_u64 v[200:201], s[24:25], 0, v[130:131]
	global_load_lds_dwordx4 v[144:145], off
	s_add_i32 m0, s61, 0x2000
	s_nop 0
	global_load_lds_dwordx4 v[200:201], off
	s_setprio 1
	s_barrier
	s_waitcnt lgkmcnt(0)
	s_waitcnt lgkmcnt(0)
	v_mfma_f32_16x16x32_bf16 v[118:121], v[216:219], v[168:171], v[118:121]
	v_mfma_f32_16x16x32_bf16 v[114:117], v[224:227], v[168:171], v[114:117]
	v_mfma_f32_16x16x32_bf16 v[102:105], v[216:219], v[176:179], v[102:105]
	v_mfma_f32_16x16x32_bf16 v[98:101], v[224:227], v[176:179], v[98:101]
	v_mfma_f32_16x16x32_bf16 v[86:89], v[216:219], v[184:187], v[86:89]
	v_mfma_f32_16x16x32_bf16 v[82:85], v[224:227], v[184:187], v[82:85]
	v_mfma_f32_16x16x32_bf16 v[70:73], v[216:219], v[192:195], v[70:73]
	v_mfma_f32_16x16x32_bf16 v[66:69], v[224:227], v[192:195], v[66:69]
	v_mfma_f32_16x16x32_bf16 v[118:121], v[220:223], v[172:175], v[118:121]
	s_mov_b32 m0, s44
	v_mfma_f32_16x16x32_bf16 v[114:117], v[228:231], v[172:175], v[114:117]
	v_lshl_add_u64 v[232:233], s[22:23], 0, v[132:133]
	v_mfma_f32_16x16x32_bf16 v[102:105], v[220:223], v[180:183], v[102:105]
	v_mfma_f32_16x16x32_bf16 v[98:101], v[228:231], v[180:183], v[98:101]
	v_mfma_f32_16x16x32_bf16 v[86:89], v[220:223], v[188:191], v[86:89]
	v_mfma_f32_16x16x32_bf16 v[82:85], v[228:231], v[188:191], v[82:85]
	v_mfma_f32_16x16x32_bf16 v[70:73], v[220:223], v[196:199], v[70:73]
	v_mfma_f32_16x16x32_bf16 v[66:69], v[228:231], v[196:199], v[66:69]
	s_setprio 0
	s_barrier
	ds_read_b128 v[168:171], v150 offset:16384
	ds_read_b128 v[172:175], v150 offset:17408
	ds_read_b128 v[176:179], v150 offset:18432
	ds_read_b128 v[180:183], v150 offset:19456
	ds_read_b128 v[184:187], v150 offset:20480
	ds_read_b128 v[188:191], v150 offset:21504
	ds_read_b128 v[192:195], v150 offset:22528
	ds_read_b128 v[196:199], v150 offset:23552
	global_load_lds_dwordx4 v[232:233], off
	v_lshl_add_u64 v[234:235], s[22:23], 0, v[136:137]
	s_mov_b32 m0, s45
	s_nop 0
	global_load_lds_dwordx4 v[234:235], off
	s_setprio 1
	s_barrier
	s_waitcnt lgkmcnt(0)
	s_waitcnt lgkmcnt(0)
	v_mfma_f32_16x16x32_bf16 v[62:65], v[152:155], v[168:171], v[62:65]
	v_mfma_f32_16x16x32_bf16 v[58:61], v[160:163], v[168:171], v[58:61]
	v_mfma_f32_16x16x32_bf16 v[46:49], v[152:155], v[176:179], v[46:49]
	v_mfma_f32_16x16x32_bf16 v[42:45], v[160:163], v[176:179], v[42:45]
	v_mfma_f32_16x16x32_bf16 v[30:33], v[152:155], v[184:187], v[30:33]
	v_mfma_f32_16x16x32_bf16 v[26:29], v[160:163], v[184:187], v[26:29]
	v_mfma_f32_16x16x32_bf16 v[14:17], v[152:155], v[192:195], v[14:17]
	v_mfma_f32_16x16x32_bf16 v[10:13], v[160:163], v[192:195], v[10:13]
	v_mfma_f32_16x16x32_bf16 v[62:65], v[156:159], v[172:175], v[62:65]
	v_mfma_f32_16x16x32_bf16 v[58:61], v[164:167], v[172:175], v[58:61]
	v_mfma_f32_16x16x32_bf16 v[46:49], v[156:159], v[180:183], v[46:49]
	v_mfma_f32_16x16x32_bf16 v[42:45], v[164:167], v[180:183], v[42:45]
	v_mfma_f32_16x16x32_bf16 v[30:33], v[156:159], v[188:191], v[30:33]
	v_mfma_f32_16x16x32_bf16 v[26:29], v[164:167], v[188:191], v[26:29]
	v_mfma_f32_16x16x32_bf16 v[14:17], v[156:159], v[196:199], v[14:17]
	v_mfma_f32_16x16x32_bf16 v[10:13], v[164:167], v[196:199], v[10:13]
	s_setprio 0
	s_barrier
; #define G8_STAGE(bufoff, gbase, voff) do { _Pragma("unroll") for (int _i = 0; _i < 2; ++_i) \
;         __builtin_amdgcn_global_load_lds((const unsigned*)((const char*)(gbase) + (voff)[_i]), (LAS unsigned*)(lds + (bufoff) + ldsw + _i * 8192), 16, 0, 0); } while (0)
; #define G8_LDA(dst, b, h) do { _Pragma("unroll") for (int m = 0; m < 4; ++m) _Pragma("unroll") for (int k = 0; k < 2; ++k) dst[m][k] = *(const LAS bf16x8*)(lds + G8_SA(b, h) + aoff + m * 2048 + k * 1024); } while (0)
; #define G8_LDB(dst, b, h) do { _Pragma("unroll") for (int n = 0; n < 2; ++n) _Pragma("unroll") for (int k = 0; k < 2; ++k) dst[n][k] = *(const LAS bf16x8*)(lds + G8_SB(b, h) + boff + n * 2048 + k * 1024); } while (0)
; #define G8_MMA(ai, bj, At, Bt) do { __builtin_amdgcn_s_setprio(1); _Pragma("unroll") for (int m = 0; m < 4; ++m) _Pragma("unroll") for (int n = 0; n < 2; ++n) _Pragma("unroll") for (int k = 0; k < 2; ++k) \
;         acc[ai][bj][m][n] = __builtin_amdgcn_mfma_f32_16x16x32_bf16(Bt[n][k], At[m][k], acc[ai][bj][m][n], 0, 0, 0); __builtin_amdgcn_s_setprio(0); } while (0)
; #define G8_WAIT_V(n) asm volatile("s_waitcnt vmcnt(" #n ")" ::: "memory")
; #define G8_WAIT_L(n) asm volatile("s_waitcnt lgkmcnt(" #n ")" ::: "memory")
; #define G8_BAR __builtin_amdgcn_s_barrier()
; #define G8_SCHED __builtin_amdgcn_sched_barrier(0)
; template <class Epi, class Sched>
; __device__ __forceinline__ void gemm_phase(LAS unsigned char* lds, const int K, const Sched& S, const Epi& E) {
;     ...
;             G8_STAGE(G8_SB(0, 1), b2 + hstep, voffB);
;             G8_WAIT_V(6); G8_BAR; G8_MMA(1, 1, At, B1); G8_BAR;
;             G8_LDB(B0, 1, 0); G8_SCHED; G8_LDA(At, 1, 0); G8_STAGE(G8_SA(0, 1), a2, oc[1]);
;             G8_WAIT_L(8); G8_BAR; G8_WAIT_L(0); G8_MMA(0, 0, At, B0); G8_BAR; G8_SCHED;
;             G8_LDB(B1, 1, 1); G8_STAGE(G8_SB(1, 0), b3, voffB);
;             G8_BAR; G8_WAIT_L(0); G8_MMA(0, 1, At, B1); G8_BAR;
;             G8_LDA(At, 1, 1); G8_STAGE(G8_SA(1, 0), a3, oc[0]);
;             G8_BAR; G8_WAIT_L(0); G8_MMA(1, 0, At, B0); G8_BAR; G8_SCHED;
	s_add_u32 s24, s24, s42
	s_addc_u32 s25, s25, 0
	s_add_i32 s61, s62, s43
	v_lshl_add_u64 v[236:237], s[24:25], 0, v[0:1]
	s_mov_b32 m0, s61
	v_lshl_add_u64 v[238:239], s[24:25], 0, v[130:131]
	global_load_lds_dwordx4 v[236:237], off
	s_add_i32 m0, s61, 0x2000
	s_nop 0
	global_load_lds_dwordx4 v[238:239], off
	s_waitcnt vmcnt(6)
	s_setprio 1
	s_barrier
	v_mfma_f32_16x16x32_bf16 v[54:57], v[216:219], v[168:171], v[54:57]
	v_mfma_f32_16x16x32_bf16 v[50:53], v[224:227], v[168:171], v[50:53]
	v_mfma_f32_16x16x32_bf16 v[38:41], v[216:219], v[176:179], v[38:41]
	v_mfma_f32_16x16x32_bf16 v[34:37], v[224:227], v[176:179], v[34:37]
	v_mfma_f32_16x16x32_bf16 v[22:25], v[216:219], v[184:187], v[22:25]
	v_mfma_f32_16x16x32_bf16 v[18:21], v[224:227], v[184:187], v[18:21]
	v_mfma_f32_16x16x32_bf16 v[6:9], v[216:219], v[192:195], v[6:9]
	v_mfma_f32_16x16x32_bf16 v[2:5], v[224:227], v[192:195], v[2:5]
	v_mfma_f32_16x16x32_bf16 v[54:57], v[220:223], v[172:175], v[54:57]
	s_add_i32 s24, 0, 0x18000
	v_mfma_f32_16x16x32_bf16 v[50:53], v[228:231], v[172:175], v[50:53]
	v_add_u32_e32 v151, s24, v148
	v_mfma_f32_16x16x32_bf16 v[38:41], v[220:223], v[180:183], v[38:41]
	v_mfma_f32_16x16x32_bf16 v[34:37], v[228:231], v[180:183], v[34:37]
	v_mfma_f32_16x16x32_bf16 v[22:25], v[220:223], v[188:191], v[22:25]
	v_mfma_f32_16x16x32_bf16 v[18:21], v[228:231], v[188:191], v[18:21]
	v_mfma_f32_16x16x32_bf16 v[6:9], v[220:223], v[196:199], v[6:9]
	v_mfma_f32_16x16x32_bf16 v[2:5], v[228:231], v[196:199], v[2:5]
	s_setprio 0
	s_barrier
	ds_read_b128 v[152:155], v151
	ds_read_b128 v[156:159], v151 offset:1024
	ds_read_b128 v[160:163], v151 offset:2048
	ds_read_b128 v[164:167], v151 offset:3072
	s_mov_b32 m0, s46
	v_lshl_add_u64 v[216:217], s[22:23], 0, v[134:135]
	ds_read_b128 v[168:171], v150 offset:32768
	ds_read_b128 v[172:175], v150 offset:33792
	ds_read_b128 v[176:179], v150 offset:34816
	ds_read_b128 v[180:183], v150 offset:35840
	ds_read_b128 v[184:187], v150 offset:36864
	ds_read_b128 v[188:191], v150 offset:37888
	ds_read_b128 v[192:195], v150 offset:38912
	ds_read_b128 v[196:199], v150 offset:39936
	global_load_lds_dwordx4 v[216:217], off
	v_lshl_add_u64 v[216:217], s[22:23], 0, v[138:139]
	s_mov_b32 m0, s47
	s_nop 0
	global_load_lds_dwordx4 v[216:217], off
	s_waitcnt lgkmcnt(8)
	s_setprio 1
	s_barrier
	s_waitcnt lgkmcnt(0)
	s_waitcnt lgkmcnt(0)
	v_mfma_f32_16x16x32_bf16 v[126:129], v[152:155], v[168:171], v[126:129]
	v_mfma_f32_16x16x32_bf16 v[122:125], v[160:163], v[168:171], v[122:125]
	v_mfma_f32_16x16x32_bf16 v[110:113], v[152:155], v[176:179], v[110:113]
	v_mfma_f32_16x16x32_bf16 v[106:109], v[160:163], v[176:179], v[106:109]
	v_mfma_f32_16x16x32_bf16 v[94:97], v[152:155], v[184:187], v[94:97]
	v_mfma_f32_16x16x32_bf16 v[90:93], v[160:163], v[184:187], v[90:93]
	v_mfma_f32_16x16x32_bf16 v[78:81], v[152:155], v[192:195], v[78:81]
	v_mfma_f32_16x16x32_bf16 v[74:77], v[160:163], v[192:195], v[74:77]
	v_mfma_f32_16x16x32_bf16 v[126:129], v[156:159], v[172:175], v[126:129]
	v_mfma_f32_16x16x32_bf16 v[122:125], v[164:167], v[172:175], v[122:125]
	v_mfma_f32_16x16x32_bf16 v[110:113], v[156:159], v[180:183], v[110:113]
	v_mfma_f32_16x16x32_bf16 v[106:109], v[164:167], v[180:183], v[106:109]
	v_mfma_f32_16x16x32_bf16 v[94:97], v[156:159], v[188:191], v[94:97]
	v_mfma_f32_16x16x32_bf16 v[90:93], v[164:167], v[188:191], v[90:93]
	v_mfma_f32_16x16x32_bf16 v[78:81], v[156:159], v[196:199], v[78:81]
	v_mfma_f32_16x16x32_bf16 v[74:77], v[164:167], v[196:199], v[74:77]
	s_setprio 0
	s_barrier
	s_add_i32 s22, 0, 0x1c000
	s_add_i32 s23, s24, s43
	v_add_u32_e32 v151, s22, v148
	v_lshl_add_u64 v[144:145], v[144:145], 0, s[18:19]
	s_mov_b32 m0, s23
	ds_read_b128 v[216:219], v151
	ds_read_b128 v[220:223], v151 offset:1024
	ds_read_b128 v[224:227], v151 offset:2048
	ds_read_b128 v[228:231], v151 offset:3072
	global_load_lds_dwordx4 v[144:145], off
	v_lshl_add_u64 v[144:145], v[200:201], 0, s[18:19]
	s_add_i32 m0, s23, 0x2000
	s_nop 0
	global_load_lds_dwordx4 v[144:145], off
	s_setprio 1
	s_barrier
	s_waitcnt lgkmcnt(0)
	s_waitcnt lgkmcnt(0)
	v_mfma_f32_16x16x32_bf16 v[118:121], v[216:219], v[168:171], v[118:121]
	v_mfma_f32_16x16x32_bf16 v[114:117], v[224:227], v[168:171], v[114:117]
	v_mfma_f32_16x16x32_bf16 v[102:105], v[216:219], v[176:179], v[102:105]
	v_mfma_f32_16x16x32_bf16 v[98:101], v[224:227], v[176:179], v[98:101]
	v_mfma_f32_16x16x32_bf16 v[86:89], v[216:219], v[184:187], v[86:89]
	v_mfma_f32_16x16x32_bf16 v[82:85], v[224:227], v[184:187], v[82:85]
	v_mfma_f32_16x16x32_bf16 v[70:73], v[216:219], v[192:195], v[70:73]
	v_mfma_f32_16x16x32_bf16 v[66:69], v[224:227], v[192:195], v[66:69]
	v_mfma_f32_16x16x32_bf16 v[118:121], v[220:223], v[172:175], v[118:121]
	s_mov_b32 m0, s48
	v_mfma_f32_16x16x32_bf16 v[114:117], v[228:231], v[172:175], v[114:117]
	v_lshl_add_u64 v[144:145], v[232:233], 0, s[18:19]
	v_mfma_f32_16x16x32_bf16 v[102:105], v[220:223], v[180:183], v[102:105]
	v_mfma_f32_16x16x32_bf16 v[98:101], v[228:231], v[180:183], v[98:101]
	v_mfma_f32_16x16x32_bf16 v[86:89], v[220:223], v[188:191], v[86:89]
	v_mfma_f32_16x16x32_bf16 v[82:85], v[228:231], v[188:191], v[82:85]
	v_mfma_f32_16x16x32_bf16 v[70:73], v[220:223], v[196:199], v[70:73]
	v_mfma_f32_16x16x32_bf16 v[66:69], v[228:231], v[196:199], v[66:69]
	s_setprio 0
	s_barrier
	ds_read_b128 v[168:171], v150 offset:49152
	ds_read_b128 v[172:175], v150 offset:50176
	ds_read_b128 v[176:179], v150 offset:51200
	ds_read_b128 v[180:183], v150 offset:52224
	ds_read_b128 v[184:187], v150 offset:53248
	ds_read_b128 v[188:191], v150 offset:54272
	ds_read_b128 v[192:195], v150 offset:55296
	ds_read_b128 v[196:199], v150 offset:56320
	global_load_lds_dwordx4 v[144:145], off
	v_lshl_add_u64 v[144:145], v[234:235], 0, s[18:19]
	s_mov_b32 m0, s49
	s_nop 0
	global_load_lds_dwordx4 v[144:145], off
	s_setprio 1
	s_barrier
; #define G8_STAGE(bufoff, gbase, voff) do { _Pragma("unroll") for (int _i = 0; _i < 2; ++_i) \
;         __builtin_amdgcn_global_load_lds((const unsigned*)((const char*)(gbase) + (voff)[_i]), (LAS unsigned*)(lds + (bufoff) + ldsw + _i * 8192), 16, 0, 0); } while (0)
; #define G8_MMA(ai, bj, At, Bt) do { __builtin_amdgcn_s_setprio(1); _Pragma("unroll") for (int m = 0; m < 4; ++m) _Pragma("unroll") for (int n = 0; n < 2; ++n) _Pragma("unroll") for (int k = 0; k < 2; ++k) \
;         acc[ai][bj][m][n] = __builtin_amdgcn_mfma_f32_16x16x32_bf16(Bt[n][k], At[m][k], acc[ai][bj][m][n], 0, 0, 0); __builtin_amdgcn_s_setprio(0); } while (0)
; #define G8_WAIT_V(n) asm volatile("s_waitcnt vmcnt(" #n ")" ::: "memory")
; #define G8_WAIT_L(n) asm volatile("s_waitcnt lgkmcnt(" #n ")" ::: "memory")
; #define G8_BAR __builtin_amdgcn_s_barrier()
; #define G8_SCHED __builtin_amdgcn_sched_barrier(0)
; template <class Epi, class Sched>
; __device__ __forceinline__ void gemm_phase(LAS unsigned char* lds, const int K, const Sched& S, const Epi& E) {
;     ...
;             G8_BAR; G8_WAIT_L(0); G8_MMA(1, 0, At, B0); G8_BAR; G8_SCHED;
;             G8_STAGE(G8_SB(1, 1), b3 + hstep, voffB);
;             G8_WAIT_V(6); G8_BAR; G8_MMA(1, 1, At, B1); G8_BAR;
;         }
	s_waitcnt lgkmcnt(0)
	s_waitcnt lgkmcnt(0)
	v_mfma_f32_16x16x32_bf16 v[62:65], v[152:155], v[168:171], v[62:65]
	v_mfma_f32_16x16x32_bf16 v[58:61], v[160:163], v[168:171], v[58:61]
	v_mfma_f32_16x16x32_bf16 v[46:49], v[152:155], v[176:179], v[46:49]
	v_mfma_f32_16x16x32_bf16 v[42:45], v[160:163], v[176:179], v[42:45]
	v_mfma_f32_16x16x32_bf16 v[30:33], v[152:155], v[184:187], v[30:33]
	v_mfma_f32_16x16x32_bf16 v[26:29], v[160:163], v[184:187], v[26:29]
	v_mfma_f32_16x16x32_bf16 v[14:17], v[152:155], v[192:195], v[14:17]
	v_mfma_f32_16x16x32_bf16 v[10:13], v[160:163], v[192:195], v[10:13]
	v_mfma_f32_16x16x32_bf16 v[62:65], v[156:159], v[172:175], v[62:65]
	v_mfma_f32_16x16x32_bf16 v[58:61], v[164:167], v[172:175], v[58:61]
	v_mfma_f32_16x16x32_bf16 v[46:49], v[156:159], v[180:183], v[46:49]
	v_mfma_f32_16x16x32_bf16 v[42:45], v[164:167], v[180:183], v[42:45]
	v_mfma_f32_16x16x32_bf16 v[30:33], v[156:159], v[188:191], v[30:33]
	v_mfma_f32_16x16x32_bf16 v[26:29], v[164:167], v[188:191], v[26:29]
	v_mfma_f32_16x16x32_bf16 v[14:17], v[156:159], v[196:199], v[14:17]
	v_mfma_f32_16x16x32_bf16 v[10:13], v[164:167], v[196:199], v[10:13]
	s_setprio 0
	s_barrier
	s_add_i32 s22, s22, s43
	v_lshl_add_u64 v[144:145], v[236:237], 0, s[18:19]
	s_mov_b32 m0, s22
	s_nop 0
	global_load_lds_dwordx4 v[144:145], off
	v_lshl_add_u64 v[144:145], v[238:239], 0, s[18:19]
	s_add_i32 m0, s22, 0x2000
	s_nop 0
	global_load_lds_dwordx4 v[144:145], off
	s_waitcnt vmcnt(6)
	s_setprio 1
	s_barrier
	v_mfma_f32_16x16x32_bf16 v[54:57], v[216:219], v[168:171], v[54:57]
	v_mfma_f32_16x16x32_bf16 v[50:53], v[224:227], v[168:171], v[50:53]
	v_mfma_f32_16x16x32_bf16 v[38:41], v[216:219], v[176:179], v[38:41]
	v_mfma_f32_16x16x32_bf16 v[34:37], v[224:227], v[176:179], v[34:37]
	v_mfma_f32_16x16x32_bf16 v[22:25], v[216:219], v[184:187], v[22:25]
	v_mfma_f32_16x16x32_bf16 v[18:21], v[224:227], v[184:187], v[18:21]
	v_mfma_f32_16x16x32_bf16 v[6:9], v[216:219], v[192:195], v[6:9]
	v_mfma_f32_16x16x32_bf16 v[2:5], v[224:227], v[192:195], v[2:5]
	v_mfma_f32_16x16x32_bf16 v[54:57], v[220:223], v[172:175], v[54:57]
	s_add_u32 s12, s12, 0x100
	v_mfma_f32_16x16x32_bf16 v[50:53], v[228:231], v[172:175], v[50:53]
	s_addc_u32 s13, s13, 0
	v_mfma_f32_16x16x32_bf16 v[38:41], v[220:223], v[180:183], v[38:41]
	s_add_u32 s58, s58, 0x100
	v_mfma_f32_16x16x32_bf16 v[34:37], v[228:231], v[180:183], v[34:37]
	s_addc_u32 s59, s59, 0
	v_mfma_f32_16x16x32_bf16 v[22:25], v[220:223], v[188:191], v[22:25]
	s_cmp_ge_u32 s60, s50
	v_mfma_f32_16x16x32_bf16 v[18:21], v[228:231], v[188:191], v[18:21]
	s_mov_b32 s22, s60
	v_mfma_f32_16x16x32_bf16 v[6:9], v[220:223], v[196:199], v[6:9]
	v_mfma_f32_16x16x32_bf16 v[2:5], v[228:231], v[196:199], v[2:5]
	s_setprio 0
	s_barrier
	s_cbranch_scc0 .LBB0_2252
; __device__ __forceinline__ unsigned cvt_pk_bf16(float lo, float hi) { unsigned r; asm volatile("v_cvt_pk_bf16_f32 %0, %1, %2" : "=v"(r) : "v"(lo), "v"(hi)); return r; }
;     __device__ __forceinline__ void init(f32x4 (&acc)[2][2][4][2], const Unit& u, int wc, int fq) const {
;         const int col0 = u.pn * BM + wc * 32 + 8 * fq;
; #pragma unroll
;         for (int b = 0; b < 2; ++b)
; #pragma unroll
;             for (int n = 0; n < 2; ++n) { const f32x4 bv = *(const f32x4*)(bias + col0 + b * HALF + 4 * n);
;     __device__ __forceinline__ void operator()(const f32x4 (&acc)[2][2][4][2], const Unit& u, int wr, int wc, int fr, int fq) const {
;         const int row0 = u.pm * BM + wr * 64 + fr, col0 = u.pn * BM + wc * 32 + 8 * fq;
; #pragma unroll
;         for (int ai = 0; ai < 2; ++ai)
; #pragma unroll
;             for (int m = 0; m < 4; ++m) { bf16_t* rowp = O + (size_t)(row0 + ai * HALF + m * 16) * ldc + col0;
; #pragma unroll
;                 for (int bj = 0; bj < 2; ++bj) { const f32x4 v0 = acc[ai][bj][m][0], v1 = acc[ai][bj][m][1];
;                     u32x4 w; w[0] = cvt_pk_bf16(v0[0], v0[1]); w[1] = cvt_pk_bf16(v0[2], v0[3]); w[2] = cvt_pk_bf16(v1[0], v1[1]); w[3] = cvt_pk_bf16(v1[2], v1[3]);
;                     *(u32x4*)(rowp + bj * HALF) = w; } }
;     }
	s_nop 0
	s_nop 0
	s_nop 0
	s_nop 0
	s_nop 0
	s_nop 0
	s_nop 0
	s_nop 0
	s_nop 0
	v_lshl_add_u32 v152, s56, 8, v147
	v_lshl_or_b32 v144, s57, 8, v149
	v_ashrrev_i32_e32 v153, 31, v152
	v_ashrrev_i32_e32 v145, 31, v144
	v_lshlrev_b64 v[154:155], 11, v[152:153]
	v_lshl_add_u64 v[154:155], s[4:5], 0, v[154:155]
	v_lshlrev_b64 v[156:157], 1, v[144:145]
	v_lshl_add_u64 v[144:145], v[154:155], 0, v[156:157]
	v_cvt_pk_bf16_f32 v126, v126, v127
	v_cvt_pk_bf16_f32 v127, v128, v129
	v_cvt_pk_bf16_f32 v128, v122, v123
	v_cvt_pk_bf16_f32 v129, v124, v125
	global_store_dwordx4 v[144:145], v[126:129], off
	v_cvt_pk_bf16_f32 v118, v118, v119
	v_cvt_pk_bf16_f32 v119, v120, v121
	v_cvt_pk_bf16_f32 v120, v114, v115
	v_or_b32_e32 v114, 16, v152
	v_ashrrev_i32_e32 v115, 31, v114
	v_lshlrev_b64 v[114:115], 11, v[114:115]
	v_lshl_add_u64 v[114:115], s[4:5], 0, v[114:115]
	v_lshl_add_u64 v[114:115], v[114:115], 0, v[156:157]
	v_cvt_pk_bf16_f32 v121, v116, v117
	global_store_dwordx4 v[144:145], v[118:121], off offset:256
	v_cvt_pk_bf16_f32 v110, v110, v111
	v_cvt_pk_bf16_f32 v111, v112, v113
	v_cvt_pk_bf16_f32 v112, v106, v107
	v_cvt_pk_bf16_f32 v113, v108, v109
	global_store_dwordx4 v[114:115], v[110:113], off
	v_cvt_pk_bf16_f32 v102, v102, v103
	v_cvt_pk_bf16_f32 v103, v104, v105
	v_cvt_pk_bf16_f32 v104, v98, v99
	v_or_b32_e32 v98, 32, v152
	v_ashrrev_i32_e32 v99, 31, v98
	v_lshlrev_b64 v[98:99], 11, v[98:99]
	v_lshl_add_u64 v[98:99], s[4:5], 0, v[98:99]
	v_lshl_add_u64 v[98:99], v[98:99], 0, v[156:157]
	v_cvt_pk_bf16_f32 v105, v100, v101
	global_store_dwordx4 v[114:115], v[102:105], off offset:256
	v_cvt_pk_bf16_f32 v94, v94, v95
	v_cvt_pk_bf16_f32 v95, v96, v97
	v_cvt_pk_bf16_f32 v96, v90, v91
	v_cvt_pk_bf16_f32 v97, v92, v93
	global_store_dwordx4 v[98:99], v[94:97], off
	v_cvt_pk_bf16_f32 v86, v86, v87
	v_cvt_pk_bf16_f32 v87, v88, v89
	v_cvt_pk_bf16_f32 v88, v82, v83
	v_or_b32_e32 v82, 48, v152
	v_ashrrev_i32_e32 v83, 31, v82
	v_lshlrev_b64 v[82:83], 11, v[82:83]
	v_lshl_add_u64 v[82:83], s[4:5], 0, v[82:83]
	v_lshl_add_u64 v[82:83], v[82:83], 0, v[156:157]
	s_mov_b64 s[0:1], 0x40000
	v_cvt_pk_bf16_f32 v89, v84, v85
	global_store_dwordx4 v[98:99], v[86:89], off offset:256
	v_cvt_pk_bf16_f32 v78, v78, v79
	v_cvt_pk_bf16_f32 v79, v80, v81
	v_cvt_pk_bf16_f32 v80, v74, v75
	v_cvt_pk_bf16_f32 v81, v76, v77
	global_store_dwordx4 v[82:83], v[78:81], off
	v_cvt_pk_bf16_f32 v70, v70, v71
	v_cvt_pk_bf16_f32 v71, v72, v73
	v_cvt_pk_bf16_f32 v72, v66, v67
	v_cvt_pk_bf16_f32 v73, v68, v69
	global_store_dwordx4 v[82:83], v[70:73], off offset:256
	v_lshl_add_u64 v[66:67], v[144:145], 0, s[0:1]
	v_cvt_pk_bf16_f32 v62, v62, v63
	v_cvt_pk_bf16_f32 v63, v64, v65
	v_cvt_pk_bf16_f32 v64, v58, v59
	v_add_co_u32_e64 v58, s[0:1], s82, v144
	v_cvt_pk_bf16_f32 v65, v60, v61
	s_and_b64 vcc, exec, vcc
	s_nop 0
	v_addc_co_u32_e64 v59, s[0:1], 0, v145, s[0:1]
	s_mov_b64 s[0:1], 0x48000
	global_store_dwordx4 v[58:59], v[62:65], off
	v_cvt_pk_bf16_f32 v54, v54, v55
	v_cvt_pk_bf16_f32 v55, v56, v57
	v_cvt_pk_bf16_f32 v56, v50, v51
	v_lshl_add_u64 v[50:51], v[144:145], 0, s[0:1]
	s_mov_b32 s0, 0x48000
	v_cvt_pk_bf16_f32 v57, v52, v53
	global_store_dwordx4 v[66:67], v[54:57], off offset:256
	v_cvt_pk_bf16_f32 v46, v46, v47
	v_cvt_pk_bf16_f32 v47, v48, v49
	v_cvt_pk_bf16_f32 v48, v42, v43
	v_add_co_u32_e64 v42, s[0:1], s0, v144
	v_cvt_pk_bf16_f32 v49, v44, v45
	s_nop 1
	v_addc_co_u32_e64 v43, s[0:1], 0, v145, s[0:1]
	s_mov_b64 s[0:1], 0x50000
	global_store_dwordx4 v[42:43], v[46:49], off
	v_cvt_pk_bf16_f32 v38, v38, v39
	v_cvt_pk_bf16_f32 v39, v40, v41
	v_cvt_pk_bf16_f32 v40, v34, v35
	v_lshl_add_u64 v[34:35], v[144:145], 0, s[0:1]
	s_mov_b32 s0, 0x50000
	v_cvt_pk_bf16_f32 v41, v36, v37
	global_store_dwordx4 v[50:51], v[38:41], off offset:256
	v_cvt_pk_bf16_f32 v30, v30, v31
	v_cvt_pk_bf16_f32 v31, v32, v33
	v_cvt_pk_bf16_f32 v32, v26, v27
	v_add_co_u32_e64 v26, s[0:1], s0, v144
	v_cvt_pk_bf16_f32 v33, v28, v29
	s_nop 1
	v_addc_co_u32_e64 v27, s[0:1], 0, v145, s[0:1]
	s_mov_b64 s[0:1], 0x58000
	global_store_dwordx4 v[26:27], v[30:33], off
	v_cvt_pk_bf16_f32 v22, v22, v23
	v_cvt_pk_bf16_f32 v23, v24, v25
	v_cvt_pk_bf16_f32 v24, v18, v19
	v_lshl_add_u64 v[18:19], v[144:145], 0, s[0:1]
	s_mov_b32 s0, 0x58000
	v_cvt_pk_bf16_f32 v25, v20, v21
	global_store_dwordx4 v[34:35], v[22:25], off offset:256
	v_cvt_pk_bf16_f32 v14, v14, v15
	v_cvt_pk_bf16_f32 v15, v16, v17
	v_cvt_pk_bf16_f32 v16, v10, v11
	v_add_co_u32_e64 v10, s[0:1], s0, v144
	v_cvt_pk_bf16_f32 v17, v12, v13
	s_nop 1
	v_addc_co_u32_e64 v11, s[0:1], 0, v145, s[0:1]
	global_store_dwordx4 v[10:11], v[14:17], off
	v_cvt_pk_bf16_f32 v6, v6, v7
	v_cvt_pk_bf16_f32 v7, v8, v9
	v_cvt_pk_bf16_f32 v8, v2, v3
	v_cvt_pk_bf16_f32 v9, v4, v5
	s_mov_b64 s[0:1], -1
	global_store_dwordx4 v[18:19], v[6:9], off offset:256
	s_cbranch_vccz .LBB0_2244
	v_lshl_or_b32 v2, s54, 8, v149
	v_ashrrev_i32_e32 v3, 31, v2
	v_lshl_add_u64 v[6:7], v[2:3], 2, s[2:3]
	global_load_dwordx4 v[10:13], v[6:7], off offset:16
	global_load_dwordx4 v[14:17], v[6:7], off
	global_load_dwordx4 v[2:5], v[6:7], off offset:528
	s_nop 0
	global_load_dwordx4 v[6:9], v[6:7], off offset:512
	s_mov_b64 s[0:1], 0
	s_branch .LBB0_2244

; #define G8_STAGE(bufoff, gbase, voff) do { _Pragma("unroll") for (int _i = 0; _i < 2; ++_i) \
;         __builtin_amdgcn_global_load_lds((const unsigned*)((const char*)(gbase) + (voff)[_i]), (LAS unsigned*)(lds + (bufoff) + ldsw + _i * 8192), 16, 0, 0); } while (0)
; #define G8_LDA(dst, b, h) do { _Pragma("unroll") for (int m = 0; m < 4; ++m) _Pragma("unroll") for (int k = 0; k < 2; ++k) dst[m][k] = *(const LAS bf16x8*)(lds + G8_SA(b, h) + aoff + m * 2048 + k * 1024); } while (0)
; #define G8_LDB(dst, b, h) do { _Pragma("unroll") for (int n = 0; n < 2; ++n) _Pragma("unroll") for (int k = 0; k < 2; ++k) dst[n][k] = *(const LAS bf16x8*)(lds + G8_SB(b, h) + boff + n * 2048 + k * 1024); } while (0)
; #define G8_MMA(ai, bj, At, Bt) do { __builtin_amdgcn_s_setprio(1); _Pragma("unroll") for (int m = 0; m < 4; ++m) _Pragma("unroll") for (int n = 0; n < 2; ++n) _Pragma("unroll") for (int k = 0; k < 2; ++k) \
;         acc[ai][bj][m][n] = __builtin_amdgcn_mfma_f32_16x16x32_bf16(Bt[n][k], At[m][k], acc[ai][bj][m][n], 0, 0, 0); __builtin_amdgcn_s_setprio(0); } while (0)
; #define G8_WAIT_V(n) asm volatile("s_waitcnt vmcnt(" #n ")" ::: "memory")
; #define G8_WAIT_L(n) asm volatile("s_waitcnt lgkmcnt(" #n ")" ::: "memory")
; template <class Epi, class Sched>
; __device__ __forceinline__ void gemm_phase(LAS unsigned char* lds, const int K, const Sched& S, const Epi& E) {
;     ...
;         for (int t = 0; t < nt; t += 2) {
;             const bool last = (t == nt - 2);
;             const char* a1 = cA + (size_t)(t + 1) * kstep;
;             const char* a2 = last ? nA : cA + (size_t)(t + 2) * kstep; const char* b2 = last ? nB : cB + (size_t)(t + 2) * kstep;
;             const char* a3 = a2 + kstep; const char* b3 = b2 + kstep;
;             G8_LDB(B0, 0, 0); G8_SCHED; G8_LDA(At, 0, 0); G8_STAGE(G8_SA(1, 1), a1, oc[1]);
;             if (last && has_next) S.aoff(nxt, tid, oc);
;             G8_WAIT_L(8); G8_BAR; G8_WAIT_L(0); G8_MMA(0, 0, At, B0); G8_BAR; G8_SCHED;
;             G8_LDB(B1, 0, 1); G8_STAGE(G8_SB(0, 0), b2, voffB);
;             G8_BAR; G8_WAIT_L(0); G8_MMA(0, 1, At, B1); G8_BAR;
;             G8_LDA(At, 0, 1); G8_STAGE(G8_SA(0, 0), a2, oc[0]);
;             G8_BAR; G8_WAIT_L(0); G8_MMA(1, 0, At, B0); G8_BAR; G8_SCHED;
;             G8_STAGE(G8_SB(0, 1), b2 + hstep, voffB);
;             G8_WAIT_V(6); G8_BAR; G8_MMA(1, 1, At, B1); G8_BAR;
.LBB0_2526:
	s_add_u32 s34, s22, 0x80
	s_waitcnt lgkmcnt(8)
	s_barrier
	s_waitcnt lgkmcnt(0)
	s_addc_u32 s35, s23, 0
	s_and_b64 s[24:25], s[24:25], exec
	s_cselect_b32 s35, s1, s35
	s_cselect_b32 s34, s0, s34
	s_cselect_b32 s25, s13, s56
	s_cselect_b32 s24, s12, s55
	s_setprio 1
	s_waitcnt lgkmcnt(0)
	v_mfma_f32_16x16x32_bf16 v[126:129], v[130:133], v[170:173], v[126:129]
	v_mfma_f32_16x16x32_bf16 v[122:125], v[138:141], v[170:173], v[122:125]
	v_mfma_f32_16x16x32_bf16 v[110:113], v[130:133], v[162:165], v[110:113]
	v_mfma_f32_16x16x32_bf16 v[106:109], v[138:141], v[162:165], v[106:109]
	v_mfma_f32_16x16x32_bf16 v[94:97], v[130:133], v[154:157], v[94:97]
	v_mfma_f32_16x16x32_bf16 v[90:93], v[138:141], v[154:157], v[90:93]
	v_mfma_f32_16x16x32_bf16 v[78:81], v[130:133], v[146:149], v[78:81]
	v_mfma_f32_16x16x32_bf16 v[74:77], v[138:141], v[146:149], v[74:77]
	v_mfma_f32_16x16x32_bf16 v[126:129], v[134:137], v[174:177], v[126:129]
	v_mfma_f32_16x16x32_bf16 v[122:125], v[142:145], v[174:177], v[122:125]
	v_mfma_f32_16x16x32_bf16 v[110:113], v[134:137], v[166:169], v[110:113]
	v_mfma_f32_16x16x32_bf16 v[106:109], v[142:145], v[166:169], v[106:109]
	v_mfma_f32_16x16x32_bf16 v[94:97], v[134:137], v[158:161], v[94:97]
	v_mfma_f32_16x16x32_bf16 v[90:93], v[142:145], v[158:161], v[90:93]
	v_mfma_f32_16x16x32_bf16 v[78:81], v[134:137], v[150:153], v[78:81]
	v_mfma_f32_16x16x32_bf16 v[74:77], v[142:145], v[150:153], v[74:77]
	s_setprio 0
	s_barrier
	s_add_i32 s60, 0, 0x14000
	s_mov_b32 m0, s43
	v_add_u32_e32 v183, s60, v198
	v_lshl_add_u64 v[232:233], s[24:25], 0, v[178:179]
	ds_read_b128 v[216:219], v183
	ds_read_b128 v[220:223], v183 offset:1024
	ds_read_b128 v[224:227], v183 offset:2048
	ds_read_b128 v[228:231], v183 offset:3072
	global_load_lds_dwordx4 v[232:233], off
	v_lshl_add_u64 v[234:235], s[24:25], 0, v[180:181]
	s_mov_b32 m0, s44
	s_nop 0
	global_load_lds_dwordx4 v[234:235], off
	s_setprio 1
	s_barrier
	s_waitcnt lgkmcnt(0)
	s_waitcnt lgkmcnt(0)
	v_mfma_f32_16x16x32_bf16 v[118:121], v[216:219], v[170:173], v[118:121]
	v_mfma_f32_16x16x32_bf16 v[114:117], v[224:227], v[170:173], v[114:117]
	v_mfma_f32_16x16x32_bf16 v[102:105], v[216:219], v[162:165], v[102:105]
	v_mfma_f32_16x16x32_bf16 v[98:101], v[224:227], v[162:165], v[98:101]
	v_mfma_f32_16x16x32_bf16 v[86:89], v[216:219], v[154:157], v[86:89]
	v_mfma_f32_16x16x32_bf16 v[82:85], v[224:227], v[154:157], v[82:85]
	v_mfma_f32_16x16x32_bf16 v[70:73], v[216:219], v[146:149], v[70:73]
	v_mfma_f32_16x16x32_bf16 v[66:69], v[224:227], v[146:149], v[66:69]
	v_mfma_f32_16x16x32_bf16 v[118:121], v[220:223], v[174:177], v[118:121]
	s_mov_b32 m0, s42
	v_mfma_f32_16x16x32_bf16 v[114:117], v[228:231], v[174:177], v[114:117]
	v_mfma_f32_16x16x32_bf16 v[102:105], v[220:223], v[166:169], v[102:105]
	v_mfma_f32_16x16x32_bf16 v[98:101], v[228:231], v[166:169], v[98:101]
	v_mfma_f32_16x16x32_bf16 v[86:89], v[220:223], v[158:161], v[86:89]
	v_mfma_f32_16x16x32_bf16 v[82:85], v[228:231], v[158:161], v[82:85]
	v_mfma_f32_16x16x32_bf16 v[70:73], v[220:223], v[150:153], v[70:73]
	v_mfma_f32_16x16x32_bf16 v[66:69], v[228:231], v[150:153], v[66:69]
	s_setprio 0
	s_barrier
	ds_read_b128 v[146:149], v200 offset:16384
	ds_read_b128 v[150:153], v200 offset:17408
	ds_read_b128 v[154:157], v200 offset:18432
	ds_read_b128 v[158:161], v200 offset:19456
	ds_read_b128 v[162:165], v200 offset:20480
	ds_read_b128 v[166:169], v200 offset:21504
	ds_read_b128 v[170:173], v200 offset:22528
	ds_read_b128 v[174:177], v200 offset:23552
	global_load_lds_dwordx4 v0, s[34:35]
	s_mov_b32 m0, s45
	v_mov_b32_e32 v183, v1
	global_load_lds_dwordx4 v182, s[34:35]
	s_barrier
	s_waitcnt lgkmcnt(0)
	v_lshl_add_u64 v[236:237], s[34:35], 0, v[0:1]
	v_lshl_add_u64 v[238:239], s[34:35], 0, v[182:183]
	s_setprio 1
	s_waitcnt lgkmcnt(0)
	v_mfma_f32_16x16x32_bf16 v[62:65], v[130:133], v[146:149], v[62:65]
	v_mfma_f32_16x16x32_bf16 v[58:61], v[138:141], v[146:149], v[58:61]
	v_mfma_f32_16x16x32_bf16 v[46:49], v[130:133], v[154:157], v[46:49]
	v_mfma_f32_16x16x32_bf16 v[42:45], v[138:141], v[154:157], v[42:45]
	v_mfma_f32_16x16x32_bf16 v[30:33], v[130:133], v[162:165], v[30:33]
	v_mfma_f32_16x16x32_bf16 v[26:29], v[138:141], v[162:165], v[26:29]
	v_mfma_f32_16x16x32_bf16 v[14:17], v[130:133], v[170:173], v[14:17]
	v_mfma_f32_16x16x32_bf16 v[10:13], v[138:141], v[170:173], v[10:13]
	v_mfma_f32_16x16x32_bf16 v[62:65], v[134:137], v[150:153], v[62:65]
	v_mfma_f32_16x16x32_bf16 v[58:61], v[142:145], v[150:153], v[58:61]
	v_mfma_f32_16x16x32_bf16 v[46:49], v[134:137], v[158:161], v[46:49]
	v_mfma_f32_16x16x32_bf16 v[42:45], v[142:145], v[158:161], v[42:45]
	v_mfma_f32_16x16x32_bf16 v[30:33], v[134:137], v[166:169], v[30:33]
	v_mfma_f32_16x16x32_bf16 v[26:29], v[142:145], v[166:169], v[26:29]
	v_mfma_f32_16x16x32_bf16 v[14:17], v[134:137], v[174:177], v[14:17]
	v_mfma_f32_16x16x32_bf16 v[10:13], v[142:145], v[174:177], v[10:13]
	s_setprio 0
	s_barrier
	s_add_u32 s58, s24, 0x40000
	s_addc_u32 s59, s25, 0
	s_add_i32 s60, s60, s41
	v_lshl_add_u64 v[130:131], s[58:59], 0, v[178:179]
	s_mov_b32 m0, s60
	s_nop 0
	global_load_lds_dwordx4 v[130:131], off
	v_lshl_add_u64 v[130:131], s[58:59], 0, v[180:181]
	s_add_i32 m0, s60, 0x2000
	s_nop 0
	global_load_lds_dwordx4 v[130:131], off
	s_waitcnt vmcnt(6)
	s_setprio 1
	s_barrier
; #define G8_STAGE(bufoff, gbase, voff) do { _Pragma("unroll") for (int _i = 0; _i < 2; ++_i) \
;         __builtin_amdgcn_global_load_lds((const unsigned*)((const char*)(gbase) + (voff)[_i]), (LAS unsigned*)(lds + (bufoff) + ldsw + _i * 8192), 16, 0, 0); } while (0)
; #define G8_LDA(dst, b, h) do { _Pragma("unroll") for (int m = 0; m < 4; ++m) _Pragma("unroll") for (int k = 0; k < 2; ++k) dst[m][k] = *(const LAS bf16x8*)(lds + G8_SA(b, h) + aoff + m * 2048 + k * 1024); } while (0)
; #define G8_LDB(dst, b, h) do { _Pragma("unroll") for (int n = 0; n < 2; ++n) _Pragma("unroll") for (int k = 0; k < 2; ++k) dst[n][k] = *(const LAS bf16x8*)(lds + G8_SB(b, h) + boff + n * 2048 + k * 1024); } while (0)
; #define G8_MMA(ai, bj, At, Bt) do { __builtin_amdgcn_s_setprio(1); _Pragma("unroll") for (int m = 0; m < 4; ++m) _Pragma("unroll") for (int n = 0; n < 2; ++n) _Pragma("unroll") for (int k = 0; k < 2; ++k) \
;         acc[ai][bj][m][n] = __builtin_amdgcn_mfma_f32_16x16x32_bf16(Bt[n][k], At[m][k], acc[ai][bj][m][n], 0, 0, 0); __builtin_amdgcn_s_setprio(0); } while (0)
; #define G8_WAIT_V(n) asm volatile("s_waitcnt vmcnt(" #n ")" ::: "memory")
; #define G8_WAIT_L(n) asm volatile("s_waitcnt lgkmcnt(" #n ")" ::: "memory")
; #define G8_BAR __builtin_amdgcn_s_barrier()
; #define G8_SCHED __builtin_amdgcn_sched_barrier(0)
; template <class Epi, class Sched>
; __device__ __forceinline__ void gemm_phase(LAS unsigned char* lds, const int K, const Sched& S, const Epi& E) {
;     ...
;             G8_WAIT_V(6); G8_BAR; G8_MMA(1, 1, At, B1); G8_BAR;
;             G8_LDB(B0, 1, 0); G8_SCHED; G8_LDA(At, 1, 0); G8_STAGE(G8_SA(0, 1), a2, oc[1]);
;             G8_WAIT_L(8); G8_BAR; G8_WAIT_L(0); G8_MMA(0, 0, At, B0); G8_BAR; G8_SCHED;
;             G8_LDB(B1, 1, 1); G8_STAGE(G8_SB(1, 0), b3, voffB);
	v_mfma_f32_16x16x32_bf16 v[54:57], v[216:219], v[146:149], v[54:57]
	v_mfma_f32_16x16x32_bf16 v[50:53], v[224:227], v[146:149], v[50:53]
	v_mfma_f32_16x16x32_bf16 v[38:41], v[216:219], v[154:157], v[38:41]
	v_mfma_f32_16x16x32_bf16 v[34:37], v[224:227], v[154:157], v[34:37]
	v_mfma_f32_16x16x32_bf16 v[22:25], v[216:219], v[162:165], v[22:25]
	v_mfma_f32_16x16x32_bf16 v[18:21], v[224:227], v[162:165], v[18:21]
	v_mfma_f32_16x16x32_bf16 v[6:9], v[216:219], v[170:173], v[6:9]
	v_mfma_f32_16x16x32_bf16 v[2:5], v[224:227], v[170:173], v[2:5]
	v_mfma_f32_16x16x32_bf16 v[54:57], v[220:223], v[150:153], v[54:57]
	s_add_i32 s58, 0, 0x18000
	v_mfma_f32_16x16x32_bf16 v[50:53], v[228:231], v[150:153], v[50:53]
	v_add_u32_e32 v142, s58, v198
	v_mfma_f32_16x16x32_bf16 v[38:41], v[220:223], v[158:161], v[38:41]
	v_mfma_f32_16x16x32_bf16 v[34:37], v[228:231], v[158:161], v[34:37]
	v_mfma_f32_16x16x32_bf16 v[22:25], v[220:223], v[166:169], v[22:25]
	v_mfma_f32_16x16x32_bf16 v[18:21], v[228:231], v[166:169], v[18:21]
	v_mfma_f32_16x16x32_bf16 v[6:9], v[220:223], v[174:177], v[6:9]
	v_mfma_f32_16x16x32_bf16 v[2:5], v[228:231], v[174:177], v[2:5]
	s_setprio 0
	s_barrier
	ds_read_b128 v[130:133], v142
	ds_read_b128 v[134:137], v142 offset:1024
	ds_read_b128 v[138:141], v142 offset:2048
	ds_read_b128 v[142:145], v142 offset:3072
	s_mov_b32 m0, s46
	v_lshl_add_u64 v[190:191], s[34:35], 0, v[190:191]
	ds_read_b128 v[146:149], v200 offset:32768
	ds_read_b128 v[150:153], v200 offset:33792
	ds_read_b128 v[154:157], v200 offset:34816
	ds_read_b128 v[158:161], v200 offset:35840
	ds_read_b128 v[162:165], v200 offset:36864
	ds_read_b128 v[166:169], v200 offset:37888
	ds_read_b128 v[170:173], v200 offset:38912
	ds_read_b128 v[174:177], v200 offset:39936
	global_load_lds_dwordx4 v[190:191], off
	v_lshl_add_u64 v[190:191], s[34:35], 0, v[186:187]
	s_mov_b32 m0, s47
	s_nop 0
	global_load_lds_dwordx4 v[190:191], off
	s_waitcnt lgkmcnt(8)
	s_setprio 1
	s_barrier
	s_waitcnt lgkmcnt(0)
	s_waitcnt lgkmcnt(0)
	v_mfma_f32_16x16x32_bf16 v[126:129], v[130:133], v[146:149], v[126:129]
	v_mfma_f32_16x16x32_bf16 v[122:125], v[138:141], v[146:149], v[122:125]
	v_mfma_f32_16x16x32_bf16 v[110:113], v[130:133], v[154:157], v[110:113]
	v_mfma_f32_16x16x32_bf16 v[106:109], v[138:141], v[154:157], v[106:109]
	v_mfma_f32_16x16x32_bf16 v[94:97], v[130:133], v[162:165], v[94:97]
	v_mfma_f32_16x16x32_bf16 v[90:93], v[138:141], v[162:165], v[90:93]
	v_mfma_f32_16x16x32_bf16 v[78:81], v[130:133], v[170:173], v[78:81]
	v_mfma_f32_16x16x32_bf16 v[74:77], v[138:141], v[170:173], v[74:77]
	v_mfma_f32_16x16x32_bf16 v[126:129], v[134:137], v[150:153], v[126:129]
	v_mfma_f32_16x16x32_bf16 v[122:125], v[142:145], v[150:153], v[122:125]
	v_mfma_f32_16x16x32_bf16 v[110:113], v[134:137], v[158:161], v[110:113]
	v_mfma_f32_16x16x32_bf16 v[106:109], v[142:145], v[158:161], v[106:109]
	v_mfma_f32_16x16x32_bf16 v[94:97], v[134:137], v[166:169], v[94:97]
	v_mfma_f32_16x16x32_bf16 v[90:93], v[142:145], v[166:169], v[90:93]
	v_mfma_f32_16x16x32_bf16 v[78:81], v[134:137], v[174:177], v[78:81]
	v_mfma_f32_16x16x32_bf16 v[74:77], v[142:145], v[174:177], v[74:77]
	s_setprio 0
	s_barrier
	s_add_i32 s34, 0, 0x1c000
	s_add_i32 s35, s58, s41
	v_add_u32_e32 v183, s34, v198
	v_lshl_add_u64 v[190:191], v[232:233], 0, s[18:19]
	s_mov_b32 m0, s35
	ds_read_b128 v[216:219], v183
	ds_read_b128 v[220:223], v183 offset:1024
	ds_read_b128 v[224:227], v183 offset:2048
	ds_read_b128 v[228:231], v183 offset:3072
	global_load_lds_dwordx4 v[190:191], off
	v_lshl_add_u64 v[190:191], v[234:235], 0, s[18:19]
	s_add_i32 m0, s35, 0x2000
	s_nop 0
	global_load_lds_dwordx4 v[190:191], off
	s_setprio 1
	s_barrier
; #define G8_STAGE(bufoff, gbase, voff) do { _Pragma("unroll") for (int _i = 0; _i < 2; ++_i) \
;         __builtin_amdgcn_global_load_lds((const unsigned*)((const char*)(gbase) + (voff)[_i]), (LAS unsigned*)(lds + (bufoff) + ldsw + _i * 8192), 16, 0, 0); } while (0)
; #define G8_LDA(dst, b, h) do { _Pragma("unroll") for (int m = 0; m < 4; ++m) _Pragma("unroll") for (int k = 0; k < 2; ++k) dst[m][k] = *(const LAS bf16x8*)(lds + G8_SA(b, h) + aoff + m * 2048 + k * 1024); } while (0)
; #define G8_MMA(ai, bj, At, Bt) do { __builtin_amdgcn_s_setprio(1); _Pragma("unroll") for (int m = 0; m < 4; ++m) _Pragma("unroll") for (int n = 0; n < 2; ++n) _Pragma("unroll") for (int k = 0; k < 2; ++k) \
;         acc[ai][bj][m][n] = __builtin_amdgcn_mfma_f32_16x16x32_bf16(Bt[n][k], At[m][k], acc[ai][bj][m][n], 0, 0, 0); __builtin_amdgcn_s_setprio(0); } while (0)
; #define G8_WAIT_V(n) asm volatile("s_waitcnt vmcnt(" #n ")" ::: "memory")
; #define G8_WAIT_L(n) asm volatile("s_waitcnt lgkmcnt(" #n ")" ::: "memory")
; #define G8_BAR __builtin_amdgcn_s_barrier()
; #define G8_SCHED __builtin_amdgcn_sched_barrier(0)
; template <class Epi, class Sched>
; __device__ __forceinline__ void gemm_phase(LAS unsigned char* lds, const int K, const Sched& S, const Epi& E) {
;     ...
;             G8_BAR; G8_WAIT_L(0); G8_MMA(0, 1, At, B1); G8_BAR;
;             G8_LDA(At, 1, 1); G8_STAGE(G8_SA(1, 0), a3, oc[0]);
;             G8_BAR; G8_WAIT_L(0); G8_MMA(1, 0, At, B0); G8_BAR; G8_SCHED;
;             G8_STAGE(G8_SB(1, 1), b3 + hstep, voffB);
;             G8_WAIT_V(6); G8_BAR; G8_MMA(1, 1, At, B1); G8_BAR;
;         }
	s_waitcnt lgkmcnt(0)
	s_waitcnt lgkmcnt(0)
	v_mfma_f32_16x16x32_bf16 v[118:121], v[216:219], v[146:149], v[118:121]
	v_mfma_f32_16x16x32_bf16 v[114:117], v[224:227], v[146:149], v[114:117]
	v_mfma_f32_16x16x32_bf16 v[102:105], v[216:219], v[154:157], v[102:105]
	v_mfma_f32_16x16x32_bf16 v[98:101], v[224:227], v[154:157], v[98:101]
	v_mfma_f32_16x16x32_bf16 v[86:89], v[216:219], v[162:165], v[86:89]
	v_mfma_f32_16x16x32_bf16 v[82:85], v[224:227], v[162:165], v[82:85]
	v_mfma_f32_16x16x32_bf16 v[70:73], v[216:219], v[170:173], v[70:73]
	v_mfma_f32_16x16x32_bf16 v[66:69], v[224:227], v[170:173], v[66:69]
	v_mfma_f32_16x16x32_bf16 v[118:121], v[220:223], v[150:153], v[118:121]
	s_mov_b32 m0, s49
	v_mfma_f32_16x16x32_bf16 v[114:117], v[228:231], v[150:153], v[114:117]
	v_lshl_add_u64 v[190:191], v[236:237], 0, s[18:19]
	v_mfma_f32_16x16x32_bf16 v[102:105], v[220:223], v[158:161], v[102:105]
	v_mfma_f32_16x16x32_bf16 v[98:101], v[228:231], v[158:161], v[98:101]
	v_mfma_f32_16x16x32_bf16 v[86:89], v[220:223], v[166:169], v[86:89]
	v_mfma_f32_16x16x32_bf16 v[82:85], v[228:231], v[166:169], v[82:85]
	v_mfma_f32_16x16x32_bf16 v[70:73], v[220:223], v[174:177], v[70:73]
	v_mfma_f32_16x16x32_bf16 v[66:69], v[228:231], v[174:177], v[66:69]
	s_setprio 0
	s_barrier
	ds_read_b128 v[146:149], v200 offset:49152
	ds_read_b128 v[150:153], v200 offset:50176
	ds_read_b128 v[154:157], v200 offset:51200
	ds_read_b128 v[158:161], v200 offset:52224
	ds_read_b128 v[162:165], v200 offset:53248
	ds_read_b128 v[166:169], v200 offset:54272
	ds_read_b128 v[170:173], v200 offset:55296
	ds_read_b128 v[174:177], v200 offset:56320
	global_load_lds_dwordx4 v[190:191], off
	v_lshl_add_u64 v[190:191], v[238:239], 0, s[18:19]
	s_mov_b32 m0, s50
	s_nop 0
	global_load_lds_dwordx4 v[190:191], off
	s_setprio 1
	s_barrier
	s_waitcnt lgkmcnt(0)
	s_waitcnt lgkmcnt(0)
	v_mfma_f32_16x16x32_bf16 v[62:65], v[130:133], v[146:149], v[62:65]
	v_mfma_f32_16x16x32_bf16 v[58:61], v[138:141], v[146:149], v[58:61]
	v_mfma_f32_16x16x32_bf16 v[46:49], v[130:133], v[154:157], v[46:49]
	v_mfma_f32_16x16x32_bf16 v[42:45], v[138:141], v[154:157], v[42:45]
	v_mfma_f32_16x16x32_bf16 v[30:33], v[130:133], v[162:165], v[30:33]
	v_mfma_f32_16x16x32_bf16 v[26:29], v[138:141], v[162:165], v[26:29]
	v_mfma_f32_16x16x32_bf16 v[14:17], v[130:133], v[170:173], v[14:17]
	v_mfma_f32_16x16x32_bf16 v[10:13], v[138:141], v[170:173], v[10:13]
	v_mfma_f32_16x16x32_bf16 v[62:65], v[134:137], v[150:153], v[62:65]
	v_mfma_f32_16x16x32_bf16 v[58:61], v[142:145], v[150:153], v[58:61]
	v_mfma_f32_16x16x32_bf16 v[46:49], v[134:137], v[158:161], v[46:49]
	v_mfma_f32_16x16x32_bf16 v[42:45], v[142:145], v[158:161], v[42:45]
	v_mfma_f32_16x16x32_bf16 v[30:33], v[134:137], v[166:169], v[30:33]
	v_mfma_f32_16x16x32_bf16 v[26:29], v[142:145], v[166:169], v[26:29]
	v_mfma_f32_16x16x32_bf16 v[14:17], v[134:137], v[174:177], v[14:17]
	v_mfma_f32_16x16x32_bf16 v[10:13], v[142:145], v[174:177], v[10:13]
	s_setprio 0
	s_barrier
	s_add_u32 s24, s24, 0x40080
	s_addc_u32 s25, s25, 0
	s_add_i32 s34, s34, s41
	v_lshl_add_u64 v[130:131], s[24:25], 0, v[178:179]
	s_mov_b32 m0, s34
	s_nop 0
	global_load_lds_dwordx4 v[130:131], off
	v_lshl_add_u64 v[130:131], s[24:25], 0, v[180:181]
	s_add_i32 m0, s34, 0x2000
	s_nop 0
	global_load_lds_dwordx4 v[130:131], off
	s_waitcnt vmcnt(6)
	s_setprio 1
	s_barrier
	v_mfma_f32_16x16x32_bf16 v[54:57], v[216:219], v[146:149], v[54:57]
	v_mfma_f32_16x16x32_bf16 v[50:53], v[224:227], v[146:149], v[50:53]
	v_mfma_f32_16x16x32_bf16 v[38:41], v[216:219], v[154:157], v[38:41]
	v_mfma_f32_16x16x32_bf16 v[34:37], v[224:227], v[154:157], v[34:37]
	v_mfma_f32_16x16x32_bf16 v[22:25], v[216:219], v[162:165], v[22:25]
	v_mfma_f32_16x16x32_bf16 v[18:21], v[224:227], v[162:165], v[18:21]
	v_mfma_f32_16x16x32_bf16 v[6:9], v[216:219], v[170:173], v[6:9]
	v_mfma_f32_16x16x32_bf16 v[2:5], v[224:227], v[170:173], v[2:5]
	v_mfma_f32_16x16x32_bf16 v[54:57], v[220:223], v[150:153], v[54:57]
	s_add_i32 s57, s57, 2
	v_mfma_f32_16x16x32_bf16 v[50:53], v[228:231], v[150:153], v[50:53]
	s_add_u32 s22, s22, 0x100
	v_mfma_f32_16x16x32_bf16 v[38:41], v[220:223], v[158:161], v[38:41]
	s_addc_u32 s23, s23, 0
	v_mfma_f32_16x16x32_bf16 v[34:37], v[228:231], v[158:161], v[34:37]
	s_add_u32 s55, s55, 0x100
	v_mfma_f32_16x16x32_bf16 v[22:25], v[220:223], v[166:169], v[22:25]
	s_addc_u32 s56, s56, 0
	v_mfma_f32_16x16x32_bf16 v[18:21], v[228:231], v[166:169], v[18:21]
	s_cmp_gt_u32 s57, 13
	v_mfma_f32_16x16x32_bf16 v[6:9], v[220:223], v[174:177], v[6:9]
	v_mfma_f32_16x16x32_bf16 v[2:5], v[228:231], v[174:177], v[2:5]
	s_setprio 0
	s_barrier
	s_cbranch_scc1 .LBB0_2529

; #define G8_STAGE(bufoff, gbase, voff) do { _Pragma("unroll") for (int _i = 0; _i < 2; ++_i) \
;         __builtin_amdgcn_global_load_lds((const unsigned*)((const char*)(gbase) + (voff)[_i]), (LAS unsigned*)(lds + (bufoff) + ldsw + _i * 8192), 16, 0, 0); } while (0)
; #define G8_LDA(dst, b, h) do { _Pragma("unroll") for (int m = 0; m < 4; ++m) _Pragma("unroll") for (int k = 0; k < 2; ++k) dst[m][k] = *(const LAS bf16x8*)(lds + G8_SA(b, h) + aoff + m * 2048 + k * 1024); } while (0)
; #define G8_LDB(dst, b, h) do { _Pragma("unroll") for (int n = 0; n < 2; ++n) _Pragma("unroll") for (int k = 0; k < 2; ++k) dst[n][k] = *(const LAS bf16x8*)(lds + G8_SB(b, h) + boff + n * 2048 + k * 1024); } while (0)
; #define G8_MMA(ai, bj, At, Bt) do { __builtin_amdgcn_s_setprio(1); _Pragma("unroll") for (int m = 0; m < 4; ++m) _Pragma("unroll") for (int n = 0; n < 2; ++n) _Pragma("unroll") for (int k = 0; k < 2; ++k) \
;         acc[ai][bj][m][n] = __builtin_amdgcn_mfma_f32_16x16x32_bf16(Bt[n][k], At[m][k], acc[ai][bj][m][n], 0, 0, 0); __builtin_amdgcn_s_setprio(0); } while (0)
; #define G8_WAIT_V(n) asm volatile("s_waitcnt vmcnt(" #n ")" ::: "memory")
; #define G8_WAIT_L(n) asm volatile("s_waitcnt lgkmcnt(" #n ")" ::: "memory")
; #define G8_BAR __builtin_amdgcn_s_barrier()
; #define G8_SCHED __builtin_amdgcn_sched_barrier(0)
; template <class Epi, class Sched>
; __device__ __forceinline__ void gemm_phase(LAS unsigned char* lds, const int K, const Sched& S, const Epi& E) {
;     ...
;             const char* a1 = cA + (size_t)(t + 1) * kstep;
;             const char* a2 = last ? nA : cA + (size_t)(t + 2) * kstep; const char* b2 = last ? nB : cB + (size_t)(t + 2) * kstep;
;             const char* a3 = a2 + kstep; const char* b3 = b2 + kstep;
;             G8_LDB(B0, 0, 0); G8_SCHED; G8_LDA(At, 0, 0); G8_STAGE(G8_SA(1, 1), a1, oc[1]);
;             if (last && has_next) S.aoff(nxt, tid, oc);
;             G8_WAIT_L(8); G8_BAR; G8_WAIT_L(0); G8_MMA(0, 0, At, B0); G8_BAR; G8_SCHED;
;             G8_LDB(B1, 0, 1); G8_STAGE(G8_SB(0, 0), b2, voffB);
;             G8_BAR; G8_WAIT_L(0); G8_MMA(0, 1, At, B1); G8_BAR;
;             G8_LDA(At, 0, 1); G8_STAGE(G8_SA(0, 0), a2, oc[0]);
;             G8_BAR; G8_WAIT_L(0); G8_MMA(1, 0, At, B0); G8_BAR; G8_SCHED;
;             G8_STAGE(G8_SB(0, 1), b2 + hstep, voffB);
;             G8_WAIT_V(6); G8_BAR; G8_MMA(1, 1, At, B1); G8_BAR;
.LBB0_2616:
	s_xor_b64 s[40:41], s[42:43], -1
	s_add_u32 s44, s44, 0x100
	s_addc_u32 s45, s45, 0
	s_and_b64 s[42:43], s[36:37], exec
	s_cselect_b32 s43, s1, s45
	s_cselect_b32 s42, s0, s44
	s_add_u32 s38, s22, s38
	s_addc_u32 s39, s23, s39
	s_add_u32 s38, s38, 0x100
	s_addc_u32 s39, s39, 0
	s_waitcnt lgkmcnt(8)
	s_barrier
	s_waitcnt lgkmcnt(0)
	s_and_b64 s[36:37], s[36:37], exec
	s_cselect_b32 s37, s35, s39
	s_cselect_b32 s36, s34, s38
	s_setprio 1
	s_waitcnt lgkmcnt(0)
	v_mfma_f32_16x16x32_bf16 v[126:129], v[130:133], v[170:173], v[126:129]
	v_mfma_f32_16x16x32_bf16 v[122:125], v[138:141], v[170:173], v[122:125]
	v_mfma_f32_16x16x32_bf16 v[110:113], v[130:133], v[162:165], v[110:113]
	v_mfma_f32_16x16x32_bf16 v[106:109], v[138:141], v[162:165], v[106:109]
	v_mfma_f32_16x16x32_bf16 v[94:97], v[130:133], v[154:157], v[94:97]
	v_mfma_f32_16x16x32_bf16 v[90:93], v[138:141], v[154:157], v[90:93]
	v_mfma_f32_16x16x32_bf16 v[78:81], v[130:133], v[146:149], v[78:81]
	v_mfma_f32_16x16x32_bf16 v[74:77], v[138:141], v[146:149], v[74:77]
	v_mfma_f32_16x16x32_bf16 v[126:129], v[134:137], v[174:177], v[126:129]
	v_mfma_f32_16x16x32_bf16 v[122:125], v[142:145], v[174:177], v[122:125]
	v_mfma_f32_16x16x32_bf16 v[110:113], v[134:137], v[166:169], v[110:113]
	v_mfma_f32_16x16x32_bf16 v[106:109], v[142:145], v[166:169], v[106:109]
	v_mfma_f32_16x16x32_bf16 v[94:97], v[134:137], v[158:161], v[94:97]
	v_mfma_f32_16x16x32_bf16 v[90:93], v[142:145], v[158:161], v[90:93]
	v_mfma_f32_16x16x32_bf16 v[78:81], v[134:137], v[150:153], v[78:81]
	v_mfma_f32_16x16x32_bf16 v[74:77], v[142:145], v[150:153], v[74:77]
	s_setprio 0
	s_barrier
	s_add_i32 s44, 0, 0x14000
	s_mov_b32 m0, s52
	v_add_u32_e32 v183, s44, v200
	v_lshl_add_u64 v[236:237], s[36:37], 0, v[178:179]
	ds_read_b128 v[220:223], v183
	ds_read_b128 v[224:227], v183 offset:1024
	ds_read_b128 v[228:231], v183 offset:2048
	ds_read_b128 v[232:235], v183 offset:3072
	global_load_lds_dwordx4 v[236:237], off
	v_lshl_add_u64 v[238:239], s[36:37], 0, v[180:181]
	s_mov_b32 m0, s53
	s_nop 0
	global_load_lds_dwordx4 v[238:239], off
	s_setprio 1
	s_barrier
	s_waitcnt lgkmcnt(0)
	s_waitcnt lgkmcnt(0)
	v_mfma_f32_16x16x32_bf16 v[118:121], v[220:223], v[170:173], v[118:121]
	v_mfma_f32_16x16x32_bf16 v[114:117], v[228:231], v[170:173], v[114:117]
	v_mfma_f32_16x16x32_bf16 v[102:105], v[220:223], v[162:165], v[102:105]
	v_mfma_f32_16x16x32_bf16 v[98:101], v[228:231], v[162:165], v[98:101]
	v_mfma_f32_16x16x32_bf16 v[86:89], v[220:223], v[154:157], v[86:89]
	v_mfma_f32_16x16x32_bf16 v[82:85], v[228:231], v[154:157], v[82:85]
	v_mfma_f32_16x16x32_bf16 v[70:73], v[220:223], v[146:149], v[70:73]
	v_mfma_f32_16x16x32_bf16 v[66:69], v[228:231], v[146:149], v[66:69]
	v_mfma_f32_16x16x32_bf16 v[118:121], v[224:227], v[174:177], v[118:121]
	s_mov_b32 m0, s51
	v_mfma_f32_16x16x32_bf16 v[114:117], v[232:235], v[174:177], v[114:117]
	v_mfma_f32_16x16x32_bf16 v[102:105], v[224:227], v[166:169], v[102:105]
	v_mfma_f32_16x16x32_bf16 v[98:101], v[232:235], v[166:169], v[98:101]
	v_mfma_f32_16x16x32_bf16 v[86:89], v[224:227], v[158:161], v[86:89]
	v_mfma_f32_16x16x32_bf16 v[82:85], v[232:235], v[158:161], v[82:85]
	v_mfma_f32_16x16x32_bf16 v[70:73], v[224:227], v[150:153], v[70:73]
	v_mfma_f32_16x16x32_bf16 v[66:69], v[232:235], v[150:153], v[66:69]
	s_setprio 0
	s_barrier
	ds_read_b128 v[146:149], v216 offset:16384
	ds_read_b128 v[150:153], v216 offset:17408
	ds_read_b128 v[154:157], v216 offset:18432
	ds_read_b128 v[158:161], v216 offset:19456
	ds_read_b128 v[162:165], v216 offset:20480
	ds_read_b128 v[166:169], v216 offset:21504
	ds_read_b128 v[170:173], v216 offset:22528
	ds_read_b128 v[174:177], v216 offset:23552
	global_load_lds_dwordx4 v182, s[42:43]
	s_mov_b32 m0, s54
	v_mov_b32_e32 v183, v1
	global_load_lds_dwordx4 v184, s[42:43]
	s_barrier
	s_waitcnt lgkmcnt(0)
	v_mov_b32_e32 v185, v1
	v_lshl_add_u64 v[240:241], s[42:43], 0, v[182:183]
	v_lshl_add_u64 v[242:243], s[42:43], 0, v[184:185]
	s_setprio 1
	s_waitcnt lgkmcnt(0)
	v_mfma_f32_16x16x32_bf16 v[62:65], v[130:133], v[146:149], v[62:65]
	v_mfma_f32_16x16x32_bf16 v[58:61], v[138:141], v[146:149], v[58:61]
	v_mfma_f32_16x16x32_bf16 v[46:49], v[130:133], v[154:157], v[46:49]
	v_mfma_f32_16x16x32_bf16 v[42:45], v[138:141], v[154:157], v[42:45]
	v_mfma_f32_16x16x32_bf16 v[30:33], v[130:133], v[162:165], v[30:33]
	v_mfma_f32_16x16x32_bf16 v[26:29], v[138:141], v[162:165], v[26:29]
	v_mfma_f32_16x16x32_bf16 v[14:17], v[130:133], v[170:173], v[14:17]
	v_mfma_f32_16x16x32_bf16 v[10:13], v[138:141], v[170:173], v[10:13]
	v_mfma_f32_16x16x32_bf16 v[62:65], v[134:137], v[150:153], v[62:65]
	v_mfma_f32_16x16x32_bf16 v[58:61], v[142:145], v[150:153], v[58:61]
	v_mfma_f32_16x16x32_bf16 v[46:49], v[134:137], v[158:161], v[46:49]
	v_mfma_f32_16x16x32_bf16 v[42:45], v[142:145], v[158:161], v[42:45]
	v_mfma_f32_16x16x32_bf16 v[30:33], v[134:137], v[166:169], v[30:33]
	v_mfma_f32_16x16x32_bf16 v[26:29], v[142:145], v[166:169], v[26:29]
	v_mfma_f32_16x16x32_bf16 v[14:17], v[134:137], v[174:177], v[14:17]
	v_mfma_f32_16x16x32_bf16 v[10:13], v[142:145], v[174:177], v[10:13]
	s_setprio 0
	s_barrier
	s_add_u32 s38, s36, 0x10000
	s_addc_u32 s39, s37, 0
	s_add_i32 s44, s44, s50
	v_lshl_add_u64 v[130:131], s[38:39], 0, v[178:179]
	s_mov_b32 m0, s44
	s_nop 0
	global_load_lds_dwordx4 v[130:131], off
	v_lshl_add_u64 v[130:131], s[38:39], 0, v[180:181]
	s_add_i32 m0, s44, 0x2000
	s_nop 0
	global_load_lds_dwordx4 v[130:131], off
	s_waitcnt vmcnt(6)
	s_setprio 1
	s_barrier
; #define G8_STAGE(bufoff, gbase, voff) do { _Pragma("unroll") for (int _i = 0; _i < 2; ++_i) \
;         __builtin_amdgcn_global_load_lds((const unsigned*)((const char*)(gbase) + (voff)[_i]), (LAS unsigned*)(lds + (bufoff) + ldsw + _i * 8192), 16, 0, 0); } while (0)
; #define G8_LDA(dst, b, h) do { _Pragma("unroll") for (int m = 0; m < 4; ++m) _Pragma("unroll") for (int k = 0; k < 2; ++k) dst[m][k] = *(const LAS bf16x8*)(lds + G8_SA(b, h) + aoff + m * 2048 + k * 1024); } while (0)
; #define G8_LDB(dst, b, h) do { _Pragma("unroll") for (int n = 0; n < 2; ++n) _Pragma("unroll") for (int k = 0; k < 2; ++k) dst[n][k] = *(const LAS bf16x8*)(lds + G8_SB(b, h) + boff + n * 2048 + k * 1024); } while (0)
; #define G8_MMA(ai, bj, At, Bt) do { __builtin_amdgcn_s_setprio(1); _Pragma("unroll") for (int m = 0; m < 4; ++m) _Pragma("unroll") for (int n = 0; n < 2; ++n) _Pragma("unroll") for (int k = 0; k < 2; ++k) \
;         acc[ai][bj][m][n] = __builtin_amdgcn_mfma_f32_16x16x32_bf16(Bt[n][k], At[m][k], acc[ai][bj][m][n], 0, 0, 0); __builtin_amdgcn_s_setprio(0); } while (0)
; #define G8_WAIT_V(n) asm volatile("s_waitcnt vmcnt(" #n ")" ::: "memory")
; #define G8_WAIT_L(n) asm volatile("s_waitcnt lgkmcnt(" #n ")" ::: "memory")
; #define G8_BAR __builtin_amdgcn_s_barrier()
; #define G8_SCHED __builtin_amdgcn_sched_barrier(0)
; template <class Epi, class Sched>
; __device__ __forceinline__ void gemm_phase(LAS unsigned char* lds, const int K, const Sched& S, const Epi& E) {
;     ...
;             G8_WAIT_V(6); G8_BAR; G8_MMA(1, 1, At, B1); G8_BAR;
;             G8_LDB(B0, 1, 0); G8_SCHED; G8_LDA(At, 1, 0); G8_STAGE(G8_SA(0, 1), a2, oc[1]);
;             G8_WAIT_L(8); G8_BAR; G8_WAIT_L(0); G8_MMA(0, 0, At, B0); G8_BAR; G8_SCHED;
;             G8_LDB(B1, 1, 1); G8_STAGE(G8_SB(1, 0), b3, voffB);
;             G8_BAR; G8_WAIT_L(0); G8_MMA(0, 1, At, B1); G8_BAR;
	v_mfma_f32_16x16x32_bf16 v[54:57], v[220:223], v[146:149], v[54:57]
	v_mfma_f32_16x16x32_bf16 v[50:53], v[228:231], v[146:149], v[50:53]
	v_mfma_f32_16x16x32_bf16 v[38:41], v[220:223], v[154:157], v[38:41]
	v_mfma_f32_16x16x32_bf16 v[34:37], v[228:231], v[154:157], v[34:37]
	v_mfma_f32_16x16x32_bf16 v[22:25], v[220:223], v[162:165], v[22:25]
	v_mfma_f32_16x16x32_bf16 v[18:21], v[228:231], v[162:165], v[18:21]
	v_mfma_f32_16x16x32_bf16 v[6:9], v[220:223], v[170:173], v[6:9]
	v_mfma_f32_16x16x32_bf16 v[2:5], v[228:231], v[170:173], v[2:5]
	v_mfma_f32_16x16x32_bf16 v[54:57], v[224:227], v[150:153], v[54:57]
	s_add_i32 s38, 0, 0x18000
	v_mfma_f32_16x16x32_bf16 v[50:53], v[232:235], v[150:153], v[50:53]
	v_add_u32_e32 v142, s38, v200
	v_mfma_f32_16x16x32_bf16 v[38:41], v[224:227], v[158:161], v[38:41]
	v_mfma_f32_16x16x32_bf16 v[34:37], v[232:235], v[158:161], v[34:37]
	v_mfma_f32_16x16x32_bf16 v[22:25], v[224:227], v[166:169], v[22:25]
	v_mfma_f32_16x16x32_bf16 v[18:21], v[232:235], v[166:169], v[18:21]
	v_mfma_f32_16x16x32_bf16 v[6:9], v[224:227], v[174:177], v[6:9]
	v_mfma_f32_16x16x32_bf16 v[2:5], v[232:235], v[174:177], v[2:5]
	s_setprio 0
	s_barrier
	ds_read_b128 v[130:133], v142
	ds_read_b128 v[134:137], v142 offset:1024
	ds_read_b128 v[138:141], v142 offset:2048
	ds_read_b128 v[142:145], v142 offset:3072
	s_mov_b32 m0, s55
	v_lshl_add_u64 v[220:221], s[42:43], 0, v[0:1]
	ds_read_b128 v[146:149], v216 offset:32768
	ds_read_b128 v[150:153], v216 offset:33792
	ds_read_b128 v[154:157], v216 offset:34816
	ds_read_b128 v[158:161], v216 offset:35840
	ds_read_b128 v[162:165], v216 offset:36864
	ds_read_b128 v[166:169], v216 offset:37888
	ds_read_b128 v[170:173], v216 offset:38912
	ds_read_b128 v[174:177], v216 offset:39936
	global_load_lds_dwordx4 v[220:221], off
	v_lshl_add_u64 v[220:221], s[42:43], 0, v[186:187]
	s_mov_b32 m0, s56
	s_nop 0
	global_load_lds_dwordx4 v[220:221], off
	s_waitcnt lgkmcnt(8)
	s_setprio 1
	s_barrier
	s_waitcnt lgkmcnt(0)
	s_waitcnt lgkmcnt(0)
	v_mfma_f32_16x16x32_bf16 v[126:129], v[130:133], v[146:149], v[126:129]
	v_mfma_f32_16x16x32_bf16 v[122:125], v[138:141], v[146:149], v[122:125]
	v_mfma_f32_16x16x32_bf16 v[110:113], v[130:133], v[154:157], v[110:113]
	v_mfma_f32_16x16x32_bf16 v[106:109], v[138:141], v[154:157], v[106:109]
	v_mfma_f32_16x16x32_bf16 v[94:97], v[130:133], v[162:165], v[94:97]
	v_mfma_f32_16x16x32_bf16 v[90:93], v[138:141], v[162:165], v[90:93]
	v_mfma_f32_16x16x32_bf16 v[78:81], v[130:133], v[170:173], v[78:81]
	v_mfma_f32_16x16x32_bf16 v[74:77], v[138:141], v[170:173], v[74:77]
	v_mfma_f32_16x16x32_bf16 v[126:129], v[134:137], v[150:153], v[126:129]
	v_mfma_f32_16x16x32_bf16 v[122:125], v[142:145], v[150:153], v[122:125]
	v_mfma_f32_16x16x32_bf16 v[110:113], v[134:137], v[158:161], v[110:113]
	v_mfma_f32_16x16x32_bf16 v[106:109], v[142:145], v[158:161], v[106:109]
	v_mfma_f32_16x16x32_bf16 v[94:97], v[134:137], v[166:169], v[94:97]
	v_mfma_f32_16x16x32_bf16 v[90:93], v[142:145], v[166:169], v[90:93]
	v_mfma_f32_16x16x32_bf16 v[78:81], v[134:137], v[174:177], v[78:81]
	v_mfma_f32_16x16x32_bf16 v[74:77], v[142:145], v[174:177], v[74:77]
	s_setprio 0
	s_barrier
	s_add_i32 s39, 0, 0x1c000
	s_add_i32 s38, s38, s50
	v_add_u32_e32 v183, s39, v200
	v_lshl_add_u64 v[236:237], v[236:237], 0, s[18:19]
	s_mov_b32 m0, s38
	ds_read_b128 v[220:223], v183
	ds_read_b128 v[224:227], v183 offset:1024
	ds_read_b128 v[228:231], v183 offset:2048
	ds_read_b128 v[232:235], v183 offset:3072
	global_load_lds_dwordx4 v[236:237], off
	v_lshl_add_u64 v[236:237], v[238:239], 0, s[18:19]
	s_add_i32 m0, s38, 0x2000
	s_nop 0
	global_load_lds_dwordx4 v[236:237], off
	s_setprio 1
	s_barrier
; #define G8_STAGE(bufoff, gbase, voff) do { _Pragma("unroll") for (int _i = 0; _i < 2; ++_i) \
;         __builtin_amdgcn_global_load_lds((const unsigned*)((const char*)(gbase) + (voff)[_i]), (LAS unsigned*)(lds + (bufoff) + ldsw + _i * 8192), 16, 0, 0); } while (0)
; #define G8_LDA(dst, b, h) do { _Pragma("unroll") for (int m = 0; m < 4; ++m) _Pragma("unroll") for (int k = 0; k < 2; ++k) dst[m][k] = *(const LAS bf16x8*)(lds + G8_SA(b, h) + aoff + m * 2048 + k * 1024); } while (0)
; #define G8_MMA(ai, bj, At, Bt) do { __builtin_amdgcn_s_setprio(1); _Pragma("unroll") for (int m = 0; m < 4; ++m) _Pragma("unroll") for (int n = 0; n < 2; ++n) _Pragma("unroll") for (int k = 0; k < 2; ++k) \
;         acc[ai][bj][m][n] = __builtin_amdgcn_mfma_f32_16x16x32_bf16(Bt[n][k], At[m][k], acc[ai][bj][m][n], 0, 0, 0); __builtin_amdgcn_s_setprio(0); } while (0)
; #define G8_WAIT_V(n) asm volatile("s_waitcnt vmcnt(" #n ")" ::: "memory")
; #define G8_WAIT_L(n) asm volatile("s_waitcnt lgkmcnt(" #n ")" ::: "memory")
; #define G8_BAR __builtin_amdgcn_s_barrier()
; #define G8_SCHED __builtin_amdgcn_sched_barrier(0)
; template <class Epi, class Sched>
; __device__ __forceinline__ void gemm_phase(LAS unsigned char* lds, const int K, const Sched& S, const Epi& E) {
;     ...
;             G8_BAR; G8_WAIT_L(0); G8_MMA(0, 1, At, B1); G8_BAR;
;             G8_LDA(At, 1, 1); G8_STAGE(G8_SA(1, 0), a3, oc[0]);
;             G8_BAR; G8_WAIT_L(0); G8_MMA(1, 0, At, B0); G8_BAR; G8_SCHED;
;             G8_STAGE(G8_SB(1, 1), b3 + hstep, voffB);
;             G8_WAIT_V(6); G8_BAR; G8_MMA(1, 1, At, B1); G8_BAR;
;         }
	s_waitcnt lgkmcnt(0)
	s_waitcnt lgkmcnt(0)
	v_mfma_f32_16x16x32_bf16 v[118:121], v[220:223], v[146:149], v[118:121]
	v_mfma_f32_16x16x32_bf16 v[114:117], v[228:231], v[146:149], v[114:117]
	v_mfma_f32_16x16x32_bf16 v[102:105], v[220:223], v[154:157], v[102:105]
	v_mfma_f32_16x16x32_bf16 v[98:101], v[228:231], v[154:157], v[98:101]
	v_mfma_f32_16x16x32_bf16 v[86:89], v[220:223], v[162:165], v[86:89]
	v_mfma_f32_16x16x32_bf16 v[82:85], v[228:231], v[162:165], v[82:85]
	v_mfma_f32_16x16x32_bf16 v[70:73], v[220:223], v[170:173], v[70:73]
	v_mfma_f32_16x16x32_bf16 v[66:69], v[228:231], v[170:173], v[66:69]
	v_mfma_f32_16x16x32_bf16 v[118:121], v[224:227], v[150:153], v[118:121]
	s_mov_b32 m0, s57
	v_mfma_f32_16x16x32_bf16 v[114:117], v[232:235], v[150:153], v[114:117]
	v_lshl_add_u64 v[236:237], v[240:241], 0, s[18:19]
	v_mfma_f32_16x16x32_bf16 v[102:105], v[224:227], v[158:161], v[102:105]
	v_mfma_f32_16x16x32_bf16 v[98:101], v[232:235], v[158:161], v[98:101]
	v_mfma_f32_16x16x32_bf16 v[86:89], v[224:227], v[166:169], v[86:89]
	v_mfma_f32_16x16x32_bf16 v[82:85], v[232:235], v[166:169], v[82:85]
	v_mfma_f32_16x16x32_bf16 v[70:73], v[224:227], v[174:177], v[70:73]
	v_mfma_f32_16x16x32_bf16 v[66:69], v[232:235], v[174:177], v[66:69]
	s_setprio 0
	s_barrier
	ds_read_b128 v[146:149], v216 offset:49152
	ds_read_b128 v[150:153], v216 offset:50176
	ds_read_b128 v[154:157], v216 offset:51200
	ds_read_b128 v[158:161], v216 offset:52224
	ds_read_b128 v[162:165], v216 offset:53248
	ds_read_b128 v[166:169], v216 offset:54272
	ds_read_b128 v[170:173], v216 offset:55296
	ds_read_b128 v[174:177], v216 offset:56320
	global_load_lds_dwordx4 v[236:237], off
	v_lshl_add_u64 v[236:237], v[242:243], 0, s[18:19]
	s_mov_b32 m0, s58
	s_nop 0
	global_load_lds_dwordx4 v[236:237], off
	s_setprio 1
	s_barrier
	s_waitcnt lgkmcnt(0)
	s_waitcnt lgkmcnt(0)
	v_mfma_f32_16x16x32_bf16 v[62:65], v[130:133], v[146:149], v[62:65]
	v_mfma_f32_16x16x32_bf16 v[58:61], v[138:141], v[146:149], v[58:61]
	v_mfma_f32_16x16x32_bf16 v[46:49], v[130:133], v[154:157], v[46:49]
	v_mfma_f32_16x16x32_bf16 v[42:45], v[138:141], v[154:157], v[42:45]
	v_mfma_f32_16x16x32_bf16 v[30:33], v[130:133], v[162:165], v[30:33]
	v_mfma_f32_16x16x32_bf16 v[26:29], v[138:141], v[162:165], v[26:29]
	v_mfma_f32_16x16x32_bf16 v[14:17], v[130:133], v[170:173], v[14:17]
	v_mfma_f32_16x16x32_bf16 v[10:13], v[138:141], v[170:173], v[10:13]
	v_mfma_f32_16x16x32_bf16 v[62:65], v[134:137], v[150:153], v[62:65]
	v_mfma_f32_16x16x32_bf16 v[58:61], v[142:145], v[150:153], v[58:61]
	v_mfma_f32_16x16x32_bf16 v[46:49], v[134:137], v[158:161], v[46:49]
	v_mfma_f32_16x16x32_bf16 v[42:45], v[142:145], v[158:161], v[42:45]
	v_mfma_f32_16x16x32_bf16 v[30:33], v[134:137], v[166:169], v[30:33]
	v_mfma_f32_16x16x32_bf16 v[26:29], v[142:145], v[166:169], v[26:29]
	v_mfma_f32_16x16x32_bf16 v[14:17], v[134:137], v[174:177], v[14:17]
	v_mfma_f32_16x16x32_bf16 v[10:13], v[142:145], v[174:177], v[10:13]
	s_setprio 0
	s_barrier
	s_add_u32 s36, s36, 0x10080
	s_addc_u32 s37, s37, 0
	s_add_i32 s38, s39, s50
	v_lshl_add_u64 v[130:131], s[36:37], 0, v[178:179]
	s_mov_b32 m0, s38
	s_nop 0
	global_load_lds_dwordx4 v[130:131], off
	v_lshl_add_u64 v[130:131], s[36:37], 0, v[180:181]
	s_add_i32 m0, s38, 0x2000
	s_nop 0
	global_load_lds_dwordx4 v[130:131], off
	s_waitcnt vmcnt(6)
	s_setprio 1
	s_barrier
	v_mfma_f32_16x16x32_bf16 v[54:57], v[220:223], v[146:149], v[54:57]
	v_mfma_f32_16x16x32_bf16 v[50:53], v[228:231], v[146:149], v[50:53]
	v_mfma_f32_16x16x32_bf16 v[38:41], v[220:223], v[154:157], v[38:41]
	v_mfma_f32_16x16x32_bf16 v[34:37], v[228:231], v[154:157], v[34:37]
	v_mfma_f32_16x16x32_bf16 v[22:25], v[220:223], v[162:165], v[22:25]
	v_mfma_f32_16x16x32_bf16 v[18:21], v[228:231], v[162:165], v[18:21]
	v_mfma_f32_16x16x32_bf16 v[6:9], v[220:223], v[170:173], v[6:9]
	v_mfma_f32_16x16x32_bf16 v[2:5], v[228:231], v[170:173], v[2:5]
	v_mfma_f32_16x16x32_bf16 v[54:57], v[224:227], v[150:153], v[54:57]
	v_mfma_f32_16x16x32_bf16 v[50:53], v[232:235], v[150:153], v[50:53]
	v_mfma_f32_16x16x32_bf16 v[38:41], v[224:227], v[158:161], v[38:41]
	v_mfma_f32_16x16x32_bf16 v[34:37], v[232:235], v[158:161], v[34:37]
	v_mfma_f32_16x16x32_bf16 v[22:25], v[224:227], v[166:169], v[22:25]
	v_mfma_f32_16x16x32_bf16 v[18:21], v[232:235], v[166:169], v[18:21]
	v_mfma_f32_16x16x32_bf16 v[6:9], v[224:227], v[174:177], v[6:9]
	v_mfma_f32_16x16x32_bf16 v[2:5], v[232:235], v[174:177], v[2:5]
	s_setprio 0
	s_mov_b64 s[42:43], 0
	s_mov_b64 s[36:37], -1
	s_and_b64 vcc, exec, s[40:41]
	s_barrier
	s_cbranch_vccnz .LBB0_2618
	s_mov_b64 s[38:39], 0x100
	s_branch .LBB0_2614
